# v10: group-0 alignment barrier moved ~110 instructions into the epilogue (its head now runs under group 1's last MFMA segment); includes v9 tile-list read hoist
# speedup vs baseline: 1.0038x; 1.0038x over previous
.LBB0_215:
	ds_read_b128 v[10:13], v175
	ds_read_b128 v[14:17], v175 offset:1024
	ds_read_b128 v[166:169], v175 offset:2048
	ds_read_b128 v[170:173], v175 offset:3072
	s_add_u32 s28, s8, 0xfffc0080
	s_addc_u32 s29, s9, -1
	s_cmp_eq_u32 s64, 12
	s_cselect_b32 s31, s13, s29
	s_cselect_b32 s30, s21, s28
	s_cselect_b32 s29, s15, s63
	s_cselect_b32 s28, s51, s62
	s_mov_b32 m0, s52
	v_lshl_add_u64 v[2:3], s[8:9], 0, v[158:159]
	ds_read_b128 v[180:183], v176
	ds_read_b128 v[184:187], v176 offset:1024
	ds_read_b128 v[188:191], v176 offset:2048
	ds_read_b128 v[192:195], v176 offset:3072
	ds_read_b128 v[196:199], v176 offset:4096
	ds_read_b128 v[200:203], v176 offset:5120
	ds_read_b128 v[204:207], v176 offset:6144
	ds_read_b128 v[208:211], v176 offset:7168
	global_load_lds_dwordx4 v[2:3], off
	v_lshl_add_u64 v[2:3], s[8:9], 0, v[160:161]
	s_mov_b32 m0, s53
	s_nop 0
	global_load_lds_dwordx4 v[2:3], off
	ds_read_b128 v[212:215], v177
	ds_read_b128 v[216:219], v177 offset:1024
	ds_read_b128 v[220:223], v177 offset:2048
	ds_read_b128 v[224:227], v177 offset:3072
	s_waitcnt vmcnt(8) lgkmcnt(0)
	s_barrier
	s_setprio 1
	v_mfma_f32_16x16x128_f8f6f4 v[138:141], v[10:17], v[180:187], v[138:141]
	v_mfma_f32_16x16x128_f8f6f4 v[134:137], v[166:173], v[180:187], v[134:137]
	v_mfma_f32_16x16x128_f8f6f4 v[122:125], v[10:17], v[188:195], v[122:125]
	v_mfma_f32_16x16x128_f8f6f4 v[118:121], v[166:173], v[188:195], v[118:121]
	v_mfma_f32_16x16x128_f8f6f4 v[98:101], v[10:17], v[196:203], v[98:101]
	v_mfma_f32_16x16x128_f8f6f4 v[90:93], v[166:173], v[196:203], v[90:93]
	v_mfma_f32_16x16x128_f8f6f4 v[70:73], v[10:17], v[204:211], v[70:73]
	v_mfma_f32_16x16x128_f8f6f4 v[58:61], v[166:173], v[204:211], v[58:61]
	v_mfma_f32_16x16x128_f8f6f4 v[146:149], v[212:219], v[180:187], v[146:149]
	v_mfma_f32_16x16x128_f8f6f4 v[142:145], v[220:227], v[180:187], v[142:145]
	v_mfma_f32_16x16x128_f8f6f4 v[130:133], v[212:219], v[188:195], v[130:133]
	v_mfma_f32_16x16x128_f8f6f4 v[126:129], v[220:227], v[188:195], v[126:129]
	v_mfma_f32_16x16x128_f8f6f4 v[114:117], v[212:219], v[196:203], v[114:117]
	v_mfma_f32_16x16x128_f8f6f4 v[110:113], v[220:227], v[196:203], v[110:113]
	v_mfma_f32_16x16x128_f8f6f4 v[82:85], v[212:219], v[204:211], v[82:85]
	v_mfma_f32_16x16x128_f8f6f4 v[78:81], v[220:227], v[204:211], v[78:81]
	s_setprio 0
	s_barrier
	ds_read_b128 v[180:183], v176 offset:16384
	ds_read_b128 v[184:187], v176 offset:17408
	ds_read_b128 v[188:191], v176 offset:18432
	ds_read_b128 v[192:195], v176 offset:19456
	ds_read_b128 v[196:199], v176 offset:20480
	ds_read_b128 v[200:203], v176 offset:21504
	ds_read_b128 v[204:207], v176 offset:22528
	ds_read_b128 v[208:211], v176 offset:23552
	s_mov_b32 m0, s54
	v_lshl_add_u64 v[6:7], s[28:29], 0, v[154:155]
	global_load_lds_dwordx4 v[6:7], off
	v_lshl_add_u64 v[8:9], s[28:29], 0, v[150:151]
	s_mov_b32 m0, s55
	s_nop 0
	global_load_lds_dwordx4 v[8:9], off
	s_mov_b32 m0, s27
	v_lshl_add_u64 v[2:3], s[30:31], 0, v[156:157]
	global_load_lds_dwordx4 v[2:3], off
	v_lshl_add_u64 v[4:5], s[30:31], 0, v[152:153]
	s_mov_b32 m0, s41
	s_nop 0
	global_load_lds_dwordx4 v[4:5], off
	s_add_u32 s66, s28, 0x40000
	s_addc_u32 s67, s29, 0
	s_mov_b32 m0, s56
	v_lshl_add_u64 v[228:229], s[66:67], 0, v[154:155]
	global_load_lds_dwordx4 v[228:229], off
	v_lshl_add_u64 v[228:229], s[66:67], 0, v[150:151]
	s_mov_b32 m0, s57
	s_nop 0
	global_load_lds_dwordx4 v[228:229], off
	s_waitcnt vmcnt(8) lgkmcnt(0)
	s_barrier
	s_setprio 1
	v_mfma_f32_16x16x128_f8f6f4 v[94:97], v[10:17], v[180:187], v[94:97]
	v_mfma_f32_16x16x128_f8f6f4 v[86:89], v[166:173], v[180:187], v[86:89]
	v_mfma_f32_16x16x128_f8f6f4 v[66:69], v[10:17], v[188:195], v[66:69]
	v_mfma_f32_16x16x128_f8f6f4 v[54:57], v[166:173], v[188:195], v[54:57]
	v_mfma_f32_16x16x128_f8f6f4 v[46:49], v[10:17], v[196:203], v[46:49]
	v_mfma_f32_16x16x128_f8f6f4 v[38:41], v[166:173], v[196:203], v[38:41]
	v_mfma_f32_16x16x128_f8f6f4 v[30:33], v[10:17], v[204:211], v[30:33]
	v_mfma_f32_16x16x128_f8f6f4 v[22:25], v[166:173], v[204:211], v[22:25]
	v_mfma_f32_16x16x128_f8f6f4 v[106:109], v[212:219], v[180:187], v[106:109]
	v_mfma_f32_16x16x128_f8f6f4 v[102:105], v[220:227], v[180:187], v[102:105]
	v_mfma_f32_16x16x128_f8f6f4 v[74:77], v[212:219], v[188:195], v[74:77]
	v_mfma_f32_16x16x128_f8f6f4 v[62:65], v[220:227], v[188:195], v[62:65]
	v_mfma_f32_16x16x128_f8f6f4 v[50:53], v[212:219], v[196:203], v[50:53]
	v_mfma_f32_16x16x128_f8f6f4 v[42:45], v[220:227], v[196:203], v[42:45]
	v_mfma_f32_16x16x128_f8f6f4 v[34:37], v[212:219], v[204:211], v[34:37]
	v_mfma_f32_16x16x128_f8f6f4 v[26:29], v[220:227], v[204:211], v[26:29]
	s_setprio 0
	s_barrier
	ds_read_b128 v[10:13], v178
	ds_read_b128 v[14:17], v178 offset:1024
	ds_read_b128 v[166:169], v178 offset:2048
	ds_read_b128 v[170:173], v178 offset:3072
	s_add_u32 s30, s30, 0x40000
	s_addc_u32 s31, s31, 0
	s_mov_b32 m0, s42
	v_lshl_add_u64 v[212:213], s[30:31], 0, v[156:157]
	ds_read_b128 v[180:183], v176 offset:32768
	ds_read_b128 v[184:187], v176 offset:33792
	ds_read_b128 v[188:191], v176 offset:34816
	ds_read_b128 v[192:195], v176 offset:35840
	ds_read_b128 v[196:199], v176 offset:36864
	ds_read_b128 v[200:203], v176 offset:37888
	ds_read_b128 v[204:207], v176 offset:38912
	ds_read_b128 v[208:211], v176 offset:39936
	global_load_lds_dwordx4 v[212:213], off
	v_lshl_add_u64 v[212:213], s[30:31], 0, v[152:153]
	s_mov_b32 m0, s43
	s_nop 0
	global_load_lds_dwordx4 v[212:213], off
	ds_read_b128 v[212:215], v179
	ds_read_b128 v[216:219], v179 offset:1024
	ds_read_b128 v[220:223], v179 offset:2048
	ds_read_b128 v[224:227], v179 offset:3072
	s_waitcnt vmcnt(8) lgkmcnt(0)
	s_barrier
	s_setprio 1
	v_mfma_f32_16x16x128_f8f6f4 v[138:141], v[10:17], v[180:187], v[138:141]
	v_mfma_f32_16x16x128_f8f6f4 v[134:137], v[166:173], v[180:187], v[134:137]
	v_mfma_f32_16x16x128_f8f6f4 v[122:125], v[10:17], v[188:195], v[122:125]
	v_mfma_f32_16x16x128_f8f6f4 v[118:121], v[166:173], v[188:195], v[118:121]
	v_mfma_f32_16x16x128_f8f6f4 v[98:101], v[10:17], v[196:203], v[98:101]
	v_mfma_f32_16x16x128_f8f6f4 v[90:93], v[166:173], v[196:203], v[90:93]
	v_mfma_f32_16x16x128_f8f6f4 v[70:73], v[10:17], v[204:211], v[70:73]
	v_mfma_f32_16x16x128_f8f6f4 v[58:61], v[166:173], v[204:211], v[58:61]
	v_mfma_f32_16x16x128_f8f6f4 v[146:149], v[212:219], v[180:187], v[146:149]
	v_mfma_f32_16x16x128_f8f6f4 v[142:145], v[220:227], v[180:187], v[142:145]
	v_mfma_f32_16x16x128_f8f6f4 v[130:133], v[212:219], v[188:195], v[130:133]
	v_mfma_f32_16x16x128_f8f6f4 v[126:129], v[220:227], v[188:195], v[126:129]
	v_mfma_f32_16x16x128_f8f6f4 v[114:117], v[212:219], v[196:203], v[114:117]
	v_mfma_f32_16x16x128_f8f6f4 v[110:113], v[220:227], v[196:203], v[110:113]
	v_mfma_f32_16x16x128_f8f6f4 v[82:85], v[212:219], v[204:211], v[82:85]
	v_mfma_f32_16x16x128_f8f6f4 v[78:81], v[220:227], v[204:211], v[78:81]
	s_setprio 0
	s_barrier
	ds_read_b128 v[180:183], v176 offset:49152
	ds_read_b128 v[184:187], v176 offset:50176
	ds_read_b128 v[188:191], v176 offset:51200
	ds_read_b128 v[192:195], v176 offset:52224
	ds_read_b128 v[196:199], v176 offset:53248
	ds_read_b128 v[200:203], v176 offset:54272
	ds_read_b128 v[204:207], v176 offset:55296
	ds_read_b128 v[208:211], v176 offset:56320
	s_mov_b32 m0, s58
	v_lshl_add_u64 v[6:7], v[6:7], 0, s[4:5]
	global_load_lds_dwordx4 v[6:7], off
	v_lshl_add_u64 v[6:7], v[8:9], 0, s[4:5]
	s_mov_b32 m0, s59
	s_nop 0
	global_load_lds_dwordx4 v[6:7], off
	s_mov_b32 m0, s44
	v_lshl_add_u64 v[2:3], v[2:3], 0, s[4:5]
	global_load_lds_dwordx4 v[2:3], off
	v_lshl_add_u64 v[2:3], v[4:5], 0, s[4:5]
	s_mov_b32 m0, s45
	s_nop 0
	global_load_lds_dwordx4 v[2:3], off
	s_add_u32 s28, s28, 0x40080
	s_addc_u32 s29, s29, 0
	s_mov_b32 m0, s60
	v_lshl_add_u64 v[2:3], s[28:29], 0, v[154:155]
	global_load_lds_dwordx4 v[2:3], off
	v_lshl_add_u64 v[2:3], s[28:29], 0, v[150:151]
	s_mov_b32 m0, s61
	s_nop 0
	global_load_lds_dwordx4 v[2:3], off
	s_waitcnt vmcnt(8) lgkmcnt(0)
	s_barrier
	s_setprio 1
	v_mfma_f32_16x16x128_f8f6f4 v[94:97], v[10:17], v[180:187], v[94:97]
	v_mfma_f32_16x16x128_f8f6f4 v[86:89], v[166:173], v[180:187], v[86:89]
	v_mfma_f32_16x16x128_f8f6f4 v[66:69], v[10:17], v[188:195], v[66:69]
	v_mfma_f32_16x16x128_f8f6f4 v[54:57], v[166:173], v[188:195], v[54:57]
	v_mfma_f32_16x16x128_f8f6f4 v[46:49], v[10:17], v[196:203], v[46:49]
	v_mfma_f32_16x16x128_f8f6f4 v[38:41], v[166:173], v[196:203], v[38:41]
	v_mfma_f32_16x16x128_f8f6f4 v[30:33], v[10:17], v[204:211], v[30:33]
	v_mfma_f32_16x16x128_f8f6f4 v[22:25], v[166:173], v[204:211], v[22:25]
	v_mfma_f32_16x16x128_f8f6f4 v[106:109], v[212:219], v[180:187], v[106:109]
	v_mfma_f32_16x16x128_f8f6f4 v[102:105], v[220:227], v[180:187], v[102:105]
	v_mfma_f32_16x16x128_f8f6f4 v[74:77], v[212:219], v[188:195], v[74:77]
	v_mfma_f32_16x16x128_f8f6f4 v[62:65], v[220:227], v[188:195], v[62:65]
	v_mfma_f32_16x16x128_f8f6f4 v[50:53], v[212:219], v[196:203], v[50:53]
	v_mfma_f32_16x16x128_f8f6f4 v[42:45], v[220:227], v[196:203], v[42:45]
	v_mfma_f32_16x16x128_f8f6f4 v[34:37], v[212:219], v[204:211], v[34:37]
	v_mfma_f32_16x16x128_f8f6f4 v[26:29], v[220:227], v[204:211], v[26:29]
	s_setprio 0
	s_add_i32 s64, s64, 2
	s_add_u32 s8, s8, 0x100
	s_addc_u32 s9, s9, 0
	s_add_u32 s62, s62, 0x100
	s_addc_u32 s63, s63, 0
	s_cmp_gt_u32 s64, 13
	s_barrier
	s_cbranch_scc0 .LBB0_215
	v_mov_b32_e32 v166, v0
	s_nop 15
	s_nop 15
	s_lshl_b32 s9, s26, 8
	v_readfirstlane_b32 s8, v166
	s_ashr_i32 s13, s8, 2
	s_andn2_b32 s13, s13, 63
	s_lshr_b32 s8, s8, 1
	s_add_i32 s13, s13, s9
	s_and_b32 s8, s8, 0x60
	s_lshl_b32 s9, s50, 8
	v_and_or_b32 v178, v166, 15, s13
	v_lshrrev_b32_e32 v166, 1, v166
	s_or_b32 s8, s8, s9
	v_and_or_b32 v168, v166, 24, s8
	v_mov_b64_e32 v[14:15], v[18:19]
	v_mov_b64_e32 v[10:11], v[18:19]
	v_mov_b64_e32 v[6:7], v[18:19]
	v_mov_b64_e32 v[2:3], v[18:19]
	v_ashrrev_i32_e32 v169, 31, v168
	v_mov_b64_e32 v[166:167], s[2:3]
	v_mov_b64_e32 v[16:17], v[20:21]
	v_mov_b64_e32 v[12:13], v[20:21]
	v_mov_b64_e32 v[8:9], v[20:21]
	v_mov_b64_e32 v[4:5], v[20:21]
	v_mad_i64_i32 v[170:171], s[8:9], v178, s49, v[166:167]
	v_lshlrev_b64 v[168:169], 1, v[168:169]
	s_waitcnt vmcnt(6)
	v_lshl_add_u64 v[170:171], v[170:171], 0, v[168:169]
	v_pk_fma_f32 v[140:141], v[140:141], s[18:19], v[16:17] op_sel_hi:[1,0,1]
	v_pk_fma_f32 v[138:139], v[138:139], s[18:19], v[14:15] op_sel_hi:[1,0,1]
	v_pk_fma_f32 v[172:173], v[136:137], s[18:19], v[12:13] op_sel_hi:[1,0,1]
	v_pk_fma_f32 v[136:137], v[134:135], s[18:19], v[10:11] op_sel_hi:[1,0,1]
	v_cvt_pk_bf16_f32 v134, v138, v139
	v_cvt_pk_bf16_f32 v135, v140, v141
	v_pk_fma_f32 v[138:139], v[144:145], s[18:19], v[4:5] op_sel_hi:[1,0,1]
	v_cvt_pk_bf16_f32 v136, v136, v137
	v_cvt_pk_bf16_f32 v137, v172, v173
	global_store_dwordx4 v[170:171], v[134:137], off
	v_pk_fma_f32 v[140:141], v[142:143], s[18:19], v[2:3] op_sel_hi:[1,0,1]
	v_pk_fma_f32 v[124:125], v[124:125], s[18:19], v[16:17] op_sel_hi:[1,0,1]
	v_pk_fma_f32 v[134:135], v[146:147], s[18:19], v[6:7] op_sel_hi:[1,0,1]
	v_pk_fma_f32 v[136:137], v[148:149], s[18:19], v[8:9] op_sel_hi:[1,0,1]
	v_cvt_pk_bf16_f32 v134, v134, v135
	v_pk_fma_f32 v[122:123], v[122:123], s[18:19], v[14:15] op_sel_hi:[1,0,1]
	v_cvt_pk_bf16_f32 v135, v136, v137
	v_cvt_pk_bf16_f32 v136, v140, v141
	v_cvt_pk_bf16_f32 v137, v138, v139
	global_store_dwordx4 v[170:171], v[134:137], off offset:256
	v_pk_fma_f32 v[100:101], v[100:101], s[18:19], v[16:17] op_sel_hi:[1,0,1]
	v_pk_fma_f32 v[98:99], v[98:99], s[18:19], v[14:15] op_sel_hi:[1,0,1]
	v_or_b32_e32 v134, 16, v178
	v_mad_i64_i32 v[134:135], s[8:9], v134, s49, v[166:167]
	v_lshl_add_u64 v[134:135], v[134:135], 0, v[168:169]
	v_pk_fma_f32 v[136:137], v[120:121], s[18:19], v[12:13] op_sel_hi:[1,0,1]
	v_pk_fma_f32 v[120:121], v[118:119], s[18:19], v[10:11] op_sel_hi:[1,0,1]
	v_cvt_pk_bf16_f32 v118, v122, v123
	v_cvt_pk_bf16_f32 v119, v124, v125
	v_pk_fma_f32 v[122:123], v[128:129], s[18:19], v[4:5] op_sel_hi:[1,0,1]
	v_cvt_pk_bf16_f32 v120, v120, v121
	v_cvt_pk_bf16_f32 v121, v136, v137
	global_store_dwordx4 v[134:135], v[118:121], off
	v_pk_fma_f32 v[124:125], v[126:127], s[18:19], v[2:3] op_sel_hi:[1,0,1]
	v_pk_fma_f32 v[72:73], v[72:73], s[18:19], v[16:17] op_sel_hi:[1,0,1]
	v_pk_fma_f32 v[118:119], v[130:131], s[18:19], v[6:7] op_sel_hi:[1,0,1]
	v_pk_fma_f32 v[120:121], v[132:133], s[18:19], v[8:9] op_sel_hi:[1,0,1]
	v_cvt_pk_bf16_f32 v118, v118, v119
	v_pk_fma_f32 v[70:71], v[70:71], s[18:19], v[14:15] op_sel_hi:[1,0,1]
	v_cvt_pk_bf16_f32 v119, v120, v121
	v_cvt_pk_bf16_f32 v120, v124, v125
	v_cvt_pk_bf16_f32 v121, v122, v123
	global_store_dwordx4 v[134:135], v[118:121], off offset:256
	v_pk_fma_f32 v[66:67], v[66:67], s[18:19], v[14:15] op_sel_hi:[1,0,1]
	v_pk_fma_f32 v[62:63], v[62:63], s[18:19], v[2:3] op_sel_hi:[1,0,1]
	v_or_b32_e32 v118, 32, v178
	v_mad_i64_i32 v[118:119], s[8:9], v118, s49, v[166:167]
	v_lshl_add_u64 v[118:119], v[118:119], 0, v[168:169]
	v_pk_fma_f32 v[120:121], v[92:93], s[18:19], v[12:13] op_sel_hi:[1,0,1]
	v_pk_fma_f32 v[92:93], v[90:91], s[18:19], v[10:11] op_sel_hi:[1,0,1]
	v_cvt_pk_bf16_f32 v90, v98, v99
	v_cvt_pk_bf16_f32 v91, v100, v101
	v_pk_fma_f32 v[98:99], v[112:113], s[18:19], v[4:5] op_sel_hi:[1,0,1]
	v_cvt_pk_bf16_f32 v92, v92, v93
	v_cvt_pk_bf16_f32 v93, v120, v121
	global_store_dwordx4 v[118:119], v[90:93], off
	v_pk_fma_f32 v[100:101], v[110:111], s[18:19], v[2:3] op_sel_hi:[1,0,1]
	v_pk_fma_f32 v[48:49], v[48:49], s[18:19], v[16:17] op_sel_hi:[1,0,1]
	v_pk_fma_f32 v[90:91], v[114:115], s[18:19], v[6:7] op_sel_hi:[1,0,1]
	v_pk_fma_f32 v[92:93], v[116:117], s[18:19], v[8:9] op_sel_hi:[1,0,1]
	v_cvt_pk_bf16_f32 v90, v90, v91
	v_pk_fma_f32 v[46:47], v[46:47], s[18:19], v[14:15] op_sel_hi:[1,0,1]
	v_cvt_pk_bf16_f32 v91, v92, v93
	v_cvt_pk_bf16_f32 v92, v100, v101
	v_cvt_pk_bf16_f32 v93, v98, v99
	global_store_dwordx4 v[118:119], v[90:93], off offset:256
	v_pk_fma_f32 v[44:45], v[44:45], s[18:19], v[4:5] op_sel_hi:[1,0,1]
	v_pk_fma_f32 v[42:43], v[42:43], s[18:19], v[2:3] op_sel_hi:[1,0,1]
	v_or_b32_e32 v90, 48, v178
	v_mad_i64_i32 v[90:91], s[8:9], v90, s49, v[166:167]
	v_lshl_add_u64 v[90:91], v[90:91], 0, v[168:169]
	v_pk_fma_f32 v[92:93], v[60:61], s[18:19], v[12:13] op_sel_hi:[1,0,1]
	v_pk_fma_f32 v[60:61], v[58:59], s[18:19], v[10:11] op_sel_hi:[1,0,1]
	v_cvt_pk_bf16_f32 v58, v70, v71
	v_cvt_pk_bf16_f32 v59, v72, v73
	v_pk_fma_f32 v[70:71], v[80:81], s[18:19], v[4:5] op_sel_hi:[1,0,1]
	v_cvt_pk_bf16_f32 v60, v60, v61
	v_cvt_pk_bf16_f32 v61, v92, v93
	global_store_dwordx4 v[90:91], v[58:61], off
	v_pk_fma_f32 v[72:73], v[78:79], s[18:19], v[2:3] op_sel_hi:[1,0,1]
	v_pk_fma_f32 v[78:79], v[86:87], s[18:19], v[10:11] op_sel_hi:[1,0,1]
	v_readfirstlane_b32 s99, v0
	s_cmpk_gt_u32 s99, 0xff
	s_cbranch_scc1 .Lz0_215
	s_barrier
.Lz0_215:
	v_pk_fma_f32 v[58:59], v[82:83], s[18:19], v[6:7] op_sel_hi:[1,0,1]
	v_pk_fma_f32 v[60:61], v[84:85], s[18:19], v[8:9] op_sel_hi:[1,0,1]
	v_cvt_pk_bf16_f32 v58, v58, v59
	v_pk_fma_f32 v[24:25], v[24:25], s[18:19], v[12:13] op_sel_hi:[1,0,1]
	v_cvt_pk_bf16_f32 v59, v60, v61
	v_cvt_pk_bf16_f32 v60, v72, v73
	v_cvt_pk_bf16_f32 v61, v70, v71
	global_store_dwordx4 v[90:91], v[58:61], off offset:256
	v_pk_fma_f32 v[72:73], v[88:89], s[18:19], v[12:13] op_sel_hi:[1,0,1]
	s_and_b64 vcc, exec, s[6:7]
	v_add_u32_e32 v58, 0x80, v178
	v_mad_i64_i32 v[58:59], s[8:9], v58, s49, v[166:167]
	v_lshl_add_u64 v[70:71], v[58:59], 0, v[168:169]
	v_pk_fma_f32 v[58:59], v[94:95], s[18:19], v[14:15] op_sel_hi:[1,0,1]
	v_pk_fma_f32 v[60:61], v[96:97], s[18:19], v[16:17] op_sel_hi:[1,0,1]
	v_cvt_pk_bf16_f32 v58, v58, v59
	v_pk_fma_f32 v[14:15], v[30:31], s[18:19], v[14:15] op_sel_hi:[1,0,1]
	v_cvt_pk_bf16_f32 v59, v60, v61
	v_cvt_pk_bf16_f32 v60, v78, v79
	v_cvt_pk_bf16_f32 v61, v72, v73
	global_store_dwordx4 v[70:71], v[58:61], off
	v_pk_fma_f32 v[72:73], v[104:105], s[18:19], v[4:5] op_sel_hi:[1,0,1]
	v_pk_fma_f32 v[78:79], v[102:103], s[18:19], v[2:3] op_sel_hi:[1,0,1]
	v_pk_fma_f32 v[58:59], v[106:107], s[18:19], v[6:7] op_sel_hi:[1,0,1]
	v_pk_fma_f32 v[60:61], v[108:109], s[18:19], v[8:9] op_sel_hi:[1,0,1]
	v_cvt_pk_bf16_f32 v58, v58, v59
	s_mov_b32 s50, s14
	v_cvt_pk_bf16_f32 v59, v60, v61
	v_cvt_pk_bf16_f32 v60, v78, v79
	v_cvt_pk_bf16_f32 v61, v72, v73
	global_store_dwordx4 v[70:71], v[58:61], off offset:256
	s_mov_b32 s26, s20
	s_mov_b64 s[28:29], s[24:25]
	v_add_u32_e32 v58, 0x90, v178
	v_mad_i64_i32 v[58:59], s[8:9], v58, s49, v[166:167]
	v_lshl_add_u64 v[58:59], v[58:59], 0, v[168:169]
	v_pk_fma_f32 v[60:61], v[68:69], s[18:19], v[16:17] op_sel_hi:[1,0,1]
	v_pk_fma_f32 v[68:69], v[56:57], s[18:19], v[12:13] op_sel_hi:[1,0,1]
	v_pk_fma_f32 v[56:57], v[54:55], s[18:19], v[10:11] op_sel_hi:[1,0,1]
	v_cvt_pk_bf16_f32 v54, v66, v67
	v_cvt_pk_bf16_f32 v55, v60, v61
	v_pk_fma_f32 v[60:61], v[64:65], s[18:19], v[4:5] op_sel_hi:[1,0,1]
	v_cvt_pk_bf16_f32 v56, v56, v57
	v_cvt_pk_bf16_f32 v57, v68, v69
	global_store_dwordx4 v[58:59], v[54:57], off
	v_pk_fma_f32 v[16:17], v[32:33], s[18:19], v[16:17] op_sel_hi:[1,0,1]
	s_mov_b64 s[30:31], s[22:23]
	v_pk_fma_f32 v[54:55], v[74:75], s[18:19], v[6:7] op_sel_hi:[1,0,1]
	v_pk_fma_f32 v[56:57], v[76:77], s[18:19], v[8:9] op_sel_hi:[1,0,1]
	v_cvt_pk_bf16_f32 v54, v54, v55
	v_readlane_b32 s72, v254, 51
	v_cvt_pk_bf16_f32 v55, v56, v57
	v_cvt_pk_bf16_f32 v56, v62, v63
	v_cvt_pk_bf16_f32 v57, v60, v61
	global_store_dwordx4 v[58:59], v[54:57], off offset:256
	v_readlane_b32 s73, v254, 52
	s_nop 0
	v_add_u32_e32 v54, 0xa0, v178
	v_mad_i64_i32 v[54:55], s[8:9], v54, s49, v[166:167]
	v_lshl_add_u64 v[54:55], v[54:55], 0, v[168:169]
	v_pk_fma_f32 v[56:57], v[40:41], s[18:19], v[12:13] op_sel_hi:[1,0,1]
	v_pk_fma_f32 v[40:41], v[38:39], s[18:19], v[10:11] op_sel_hi:[1,0,1]
	v_cvt_pk_bf16_f32 v38, v46, v47
	v_cvt_pk_bf16_f32 v39, v48, v49
	v_pk_fma_f32 v[12:13], v[22:23], s[18:19], v[10:11] op_sel_hi:[1,0,1]
	v_cvt_pk_bf16_f32 v40, v40, v41
	v_cvt_pk_bf16_f32 v41, v56, v57
	global_store_dwordx4 v[54:55], v[38:41], off
	s_nop 1
	v_pk_fma_f32 v[38:39], v[50:51], s[18:19], v[6:7] op_sel_hi:[1,0,1]
	v_pk_fma_f32 v[40:41], v[52:53], s[18:19], v[8:9] op_sel_hi:[1,0,1]
	v_cvt_pk_bf16_f32 v38, v38, v39
	v_pk_fma_f32 v[8:9], v[36:37], s[18:19], v[8:9] op_sel_hi:[1,0,1]
	v_cvt_pk_bf16_f32 v39, v40, v41
	v_cvt_pk_bf16_f32 v40, v42, v43
	v_cvt_pk_bf16_f32 v41, v44, v45
	global_store_dwordx4 v[54:55], v[38:41], off offset:256
	v_cvt_pk_bf16_f32 v10, v14, v15
	v_cvt_pk_bf16_f32 v11, v16, v17
	v_cvt_pk_bf16_f32 v12, v12, v13
	v_cvt_pk_bf16_f32 v13, v24, v25
	v_pk_fma_f32 v[6:7], v[34:35], s[18:19], v[6:7] op_sel_hi:[1,0,1]
	s_nop 0
	v_add_u32_e32 v38, 0xb0, v178
	v_mad_i64_i32 v[38:39], s[8:9], v38, s49, v[166:167]
	v_lshl_add_u64 v[38:39], v[38:39], 0, v[168:169]
	global_store_dwordx4 v[38:39], v[10:13], off
	s_nop 1
	v_pk_fma_f32 v[10:11], v[28:29], s[18:19], v[4:5] op_sel_hi:[1,0,1]
	v_pk_fma_f32 v[4:5], v[26:27], s[18:19], v[2:3] op_sel_hi:[1,0,1]
	v_cvt_pk_bf16_f32 v2, v6, v7
	v_cvt_pk_bf16_f32 v3, v8, v9
	s_nop 0
	v_cvt_pk_bf16_f32 v4, v4, v5
	v_cvt_pk_bf16_f32 v5, v10, v11
	global_store_dwordx4 v[38:39], v[2:5], off offset:256
	v_readfirstlane_b32 s99, v0
	s_cmpk_gt_u32 s99, 0xff
	s_cbranch_scc0 .Lz1_215
	s_barrier

.LBB0_1106:
	ds_read_b128 v[168:171], v164
	ds_read_b128 v[172:175], v164 offset:1024
	ds_read_b128 v[176:179], v164 offset:2048
	ds_read_b128 v[180:183], v164 offset:3072
	s_add_u32 s30, s28, 0xfff80080
	s_addc_u32 s31, s29, -1
	s_cmp_eq_u32 s64, 28
	s_cselect_b32 s35, s7, s31
	s_cselect_b32 s34, s60, s30
	s_cselect_b32 s31, s21, s63
	s_cselect_b32 s30, s61, s62
	v_lshl_add_u64 v[162:163], s[28:29], 0, v[154:155]
	s_add_i32 m0, s45, 0xc000
	ds_read_b128 v[184:187], v165
	ds_read_b128 v[188:191], v165 offset:1024
	ds_read_b128 v[192:195], v165 offset:2048
	ds_read_b128 v[196:199], v165 offset:3072
	ds_read_b128 v[200:203], v165 offset:4096
	ds_read_b128 v[204:207], v165 offset:5120
	ds_read_b128 v[208:211], v165 offset:6144
	ds_read_b128 v[212:215], v165 offset:7168
	global_load_lds_dwordx4 v[162:163], off
	v_lshl_add_u64 v[162:163], s[28:29], 0, v[156:157]
	s_add_i32 m0, s45, 0xe000
	s_nop 0
	global_load_lds_dwordx4 v[162:163], off
	s_waitcnt lgkmcnt(8)
	s_barrier
	s_waitcnt lgkmcnt(0)
	s_setprio 1
	s_waitcnt lgkmcnt(0)
	v_mfma_f32_16x16x32_bf16 v[142:145], v[168:171], v[184:187], v[142:145]
	v_mfma_f32_16x16x32_bf16 v[138:141], v[176:179], v[184:187], v[138:141]
	v_mfma_f32_16x16x32_bf16 v[126:129], v[168:171], v[192:195], v[126:129]
	v_mfma_f32_16x16x32_bf16 v[122:125], v[176:179], v[192:195], v[122:125]
	v_mfma_f32_16x16x32_bf16 v[110:113], v[168:171], v[200:203], v[110:113]
	v_mfma_f32_16x16x32_bf16 v[106:109], v[176:179], v[200:203], v[106:109]
	v_mfma_f32_16x16x32_bf16 v[94:97], v[168:171], v[208:211], v[94:97]
	v_mfma_f32_16x16x32_bf16 v[90:93], v[176:179], v[208:211], v[90:93]
	v_mfma_f32_16x16x32_bf16 v[142:145], v[172:175], v[188:191], v[142:145]
	v_mfma_f32_16x16x32_bf16 v[138:141], v[180:183], v[188:191], v[138:141]
	v_mfma_f32_16x16x32_bf16 v[126:129], v[172:175], v[196:199], v[126:129]
	v_mfma_f32_16x16x32_bf16 v[122:125], v[180:183], v[196:199], v[122:125]
	v_mfma_f32_16x16x32_bf16 v[110:113], v[172:175], v[204:207], v[110:113]
	v_mfma_f32_16x16x32_bf16 v[106:109], v[180:183], v[204:207], v[106:109]
	v_mfma_f32_16x16x32_bf16 v[94:97], v[172:175], v[212:215], v[94:97]
	v_mfma_f32_16x16x32_bf16 v[90:93], v[180:183], v[212:215], v[90:93]
	s_setprio 0
	s_barrier
	s_add_i32 s65, s53, s44
	v_lshl_add_u64 v[162:163], s[30:31], 0, v[148:149]
	s_mov_b32 m0, s65
	ds_read_b128 v[216:219], v166
	ds_read_b128 v[220:223], v166 offset:1024
	ds_read_b128 v[224:227], v166 offset:2048
	ds_read_b128 v[228:231], v166 offset:3072
	global_load_lds_dwordx4 v[162:163], off
	v_lshl_add_u64 v[232:233], s[30:31], 0, v[152:153]
	s_add_i32 m0, s65, 0x2000
	s_nop 0
	global_load_lds_dwordx4 v[232:233], off
	s_barrier
	s_waitcnt lgkmcnt(0)
	s_setprio 1
	s_waitcnt lgkmcnt(0)
	v_mfma_f32_16x16x32_bf16 v[134:137], v[216:219], v[184:187], v[134:137]
	v_mfma_f32_16x16x32_bf16 v[130:133], v[224:227], v[184:187], v[130:133]
	v_mfma_f32_16x16x32_bf16 v[118:121], v[216:219], v[192:195], v[118:121]
	v_mfma_f32_16x16x32_bf16 v[114:117], v[224:227], v[192:195], v[114:117]
	v_mfma_f32_16x16x32_bf16 v[102:105], v[216:219], v[200:203], v[102:105]
	v_mfma_f32_16x16x32_bf16 v[98:101], v[224:227], v[200:203], v[98:101]
	v_mfma_f32_16x16x32_bf16 v[86:89], v[216:219], v[208:211], v[86:89]
	v_mfma_f32_16x16x32_bf16 v[82:85], v[224:227], v[208:211], v[82:85]
	v_mfma_f32_16x16x32_bf16 v[134:137], v[220:223], v[188:191], v[134:137]
	v_mfma_f32_16x16x32_bf16 v[130:133], v[228:231], v[188:191], v[130:133]
	v_mfma_f32_16x16x32_bf16 v[118:121], v[220:223], v[196:199], v[118:121]
	v_mfma_f32_16x16x32_bf16 v[114:117], v[228:231], v[196:199], v[114:117]
	v_mfma_f32_16x16x32_bf16 v[102:105], v[220:223], v[204:207], v[102:105]
	v_mfma_f32_16x16x32_bf16 v[98:101], v[228:231], v[204:207], v[98:101]
	v_mfma_f32_16x16x32_bf16 v[86:89], v[220:223], v[212:215], v[86:89]
	v_mfma_f32_16x16x32_bf16 v[82:85], v[228:231], v[212:215], v[82:85]
	s_setprio 0
	s_mov_b32 m0, s45
	v_lshl_add_u64 v[234:235], s[34:35], 0, v[146:147]
	s_barrier
	ds_read_b128 v[184:187], v165 offset:16384
	ds_read_b128 v[188:191], v165 offset:17408
	ds_read_b128 v[192:195], v165 offset:18432
	ds_read_b128 v[196:199], v165 offset:19456
	ds_read_b128 v[200:203], v165 offset:20480
	ds_read_b128 v[204:207], v165 offset:21504
	ds_read_b128 v[208:211], v165 offset:22528
	ds_read_b128 v[212:215], v165 offset:23552
	global_load_lds_dwordx4 v[234:235], off
	v_lshl_add_u64 v[236:237], s[34:35], 0, v[150:151]
	s_mov_b32 m0, s46
	s_nop 0
	global_load_lds_dwordx4 v[236:237], off
	s_barrier
	s_waitcnt lgkmcnt(0)
	s_setprio 1
	s_waitcnt lgkmcnt(0)
	v_mfma_f32_16x16x32_bf16 v[78:81], v[168:171], v[184:187], v[78:81]
	v_mfma_f32_16x16x32_bf16 v[74:77], v[176:179], v[184:187], v[74:77]
	v_mfma_f32_16x16x32_bf16 v[66:69], v[168:171], v[192:195], v[66:69]
	v_mfma_f32_16x16x32_bf16 v[58:61], v[176:179], v[192:195], v[58:61]
	v_mfma_f32_16x16x32_bf16 v[50:53], v[168:171], v[200:203], v[50:53]
	v_mfma_f32_16x16x32_bf16 v[42:45], v[176:179], v[200:203], v[42:45]
	v_mfma_f32_16x16x32_bf16 v[34:37], v[168:171], v[208:211], v[34:37]
	v_mfma_f32_16x16x32_bf16 v[26:29], v[176:179], v[208:211], v[26:29]
	v_mfma_f32_16x16x32_bf16 v[78:81], v[172:175], v[188:191], v[78:81]
	v_mfma_f32_16x16x32_bf16 v[74:77], v[180:183], v[188:191], v[74:77]
	v_mfma_f32_16x16x32_bf16 v[66:69], v[172:175], v[196:199], v[66:69]
	v_mfma_f32_16x16x32_bf16 v[58:61], v[180:183], v[196:199], v[58:61]
	v_mfma_f32_16x16x32_bf16 v[50:53], v[172:175], v[204:207], v[50:53]
	v_mfma_f32_16x16x32_bf16 v[42:45], v[180:183], v[204:207], v[42:45]
	v_mfma_f32_16x16x32_bf16 v[34:37], v[172:175], v[212:215], v[34:37]
	v_mfma_f32_16x16x32_bf16 v[26:29], v[180:183], v[212:215], v[26:29]
	s_setprio 0
	s_barrier
	s_add_u32 s66, s30, 0x80000
	s_addc_u32 s67, s31, 0
	s_add_i32 s65, s54, s44
	v_lshl_add_u64 v[168:169], s[66:67], 0, v[148:149]
	s_mov_b32 m0, s65
	s_nop 0
	global_load_lds_dwordx4 v[168:169], off
	v_lshl_add_u64 v[168:169], s[66:67], 0, v[152:153]
	s_add_i32 m0, s65, 0x2000
	s_nop 0
	global_load_lds_dwordx4 v[168:169], off
	s_waitcnt vmcnt(6)
	s_barrier
	s_setprio 1
	v_mfma_f32_16x16x32_bf16 v[70:73], v[216:219], v[184:187], v[70:73]
	v_mfma_f32_16x16x32_bf16 v[62:65], v[224:227], v[184:187], v[62:65]
	v_mfma_f32_16x16x32_bf16 v[54:57], v[216:219], v[192:195], v[54:57]
	v_mfma_f32_16x16x32_bf16 v[46:49], v[224:227], v[192:195], v[46:49]
	v_mfma_f32_16x16x32_bf16 v[38:41], v[216:219], v[200:203], v[38:41]
	v_mfma_f32_16x16x32_bf16 v[30:33], v[224:227], v[200:203], v[30:33]
	v_mfma_f32_16x16x32_bf16 v[22:25], v[216:219], v[208:211], v[22:25]
	v_mfma_f32_16x16x32_bf16 v[18:21], v[224:227], v[208:211], v[18:21]
	v_mfma_f32_16x16x32_bf16 v[70:73], v[220:223], v[188:191], v[70:73]
	v_mfma_f32_16x16x32_bf16 v[62:65], v[228:231], v[188:191], v[62:65]
	v_mfma_f32_16x16x32_bf16 v[54:57], v[220:223], v[196:199], v[54:57]
	v_mfma_f32_16x16x32_bf16 v[46:49], v[228:231], v[196:199], v[46:49]
	v_mfma_f32_16x16x32_bf16 v[38:41], v[220:223], v[204:207], v[38:41]
	v_mfma_f32_16x16x32_bf16 v[30:33], v[228:231], v[204:207], v[30:33]
	v_mfma_f32_16x16x32_bf16 v[22:25], v[220:223], v[212:215], v[22:25]
	v_mfma_f32_16x16x32_bf16 v[18:21], v[228:231], v[212:215], v[18:21]
	s_setprio 0
	s_add_i32 s65, 0, 0x18000
	v_add_u32_e32 v167, s65, v1
	s_barrier
	ds_read_b128 v[168:171], v167
	ds_read_b128 v[172:175], v167 offset:1024
	ds_read_b128 v[176:179], v167 offset:2048
	ds_read_b128 v[180:183], v167 offset:3072
	s_add_u32 s34, s34, 0x80000
	s_addc_u32 s35, s35, 0
	s_mov_b32 m0, s47
	v_lshl_add_u64 v[216:217], s[34:35], 0, v[146:147]
	ds_read_b128 v[184:187], v165 offset:32768
	ds_read_b128 v[188:191], v165 offset:33792
	ds_read_b128 v[192:195], v165 offset:34816
	ds_read_b128 v[196:199], v165 offset:35840
	ds_read_b128 v[200:203], v165 offset:36864
	ds_read_b128 v[204:207], v165 offset:37888
	ds_read_b128 v[208:211], v165 offset:38912
	ds_read_b128 v[212:215], v165 offset:39936
	global_load_lds_dwordx4 v[216:217], off
	v_lshl_add_u64 v[216:217], s[34:35], 0, v[150:151]
	s_mov_b32 m0, s48
	s_nop 0
	global_load_lds_dwordx4 v[216:217], off
	s_waitcnt lgkmcnt(8)
	s_barrier
	s_waitcnt lgkmcnt(0)
	s_setprio 1
	s_waitcnt lgkmcnt(0)
	v_mfma_f32_16x16x32_bf16 v[142:145], v[168:171], v[184:187], v[142:145]
	v_mfma_f32_16x16x32_bf16 v[138:141], v[176:179], v[184:187], v[138:141]
	v_mfma_f32_16x16x32_bf16 v[126:129], v[168:171], v[192:195], v[126:129]
	v_mfma_f32_16x16x32_bf16 v[122:125], v[176:179], v[192:195], v[122:125]
	v_mfma_f32_16x16x32_bf16 v[110:113], v[168:171], v[200:203], v[110:113]
	v_mfma_f32_16x16x32_bf16 v[106:109], v[176:179], v[200:203], v[106:109]
	v_mfma_f32_16x16x32_bf16 v[94:97], v[168:171], v[208:211], v[94:97]
	v_mfma_f32_16x16x32_bf16 v[90:93], v[176:179], v[208:211], v[90:93]
	v_mfma_f32_16x16x32_bf16 v[142:145], v[172:175], v[188:191], v[142:145]
	v_mfma_f32_16x16x32_bf16 v[138:141], v[180:183], v[188:191], v[138:141]
	v_mfma_f32_16x16x32_bf16 v[126:129], v[172:175], v[196:199], v[126:129]
	v_mfma_f32_16x16x32_bf16 v[122:125], v[180:183], v[196:199], v[122:125]
	v_mfma_f32_16x16x32_bf16 v[110:113], v[172:175], v[204:207], v[110:113]
	v_mfma_f32_16x16x32_bf16 v[106:109], v[180:183], v[204:207], v[106:109]
	v_mfma_f32_16x16x32_bf16 v[94:97], v[172:175], v[212:215], v[94:97]
	v_mfma_f32_16x16x32_bf16 v[90:93], v[180:183], v[212:215], v[90:93]
	s_setprio 0
	s_barrier
	s_add_i32 s34, 0, 0x1c000
	s_add_i32 s35, s65, s44
	v_add_u32_e32 v167, s34, v1
	v_lshl_add_u64 v[162:163], v[162:163], 0, s[10:11]
	s_mov_b32 m0, s35
	ds_read_b128 v[216:219], v167
	ds_read_b128 v[220:223], v167 offset:1024
	ds_read_b128 v[224:227], v167 offset:2048
	ds_read_b128 v[228:231], v167 offset:3072
	global_load_lds_dwordx4 v[162:163], off
	v_lshl_add_u64 v[162:163], v[232:233], 0, s[10:11]
	s_add_i32 m0, s35, 0x2000
	s_nop 0
	global_load_lds_dwordx4 v[162:163], off
	s_barrier
	s_waitcnt lgkmcnt(0)
	s_setprio 1
	s_waitcnt lgkmcnt(0)
	v_mfma_f32_16x16x32_bf16 v[134:137], v[216:219], v[184:187], v[134:137]
	v_mfma_f32_16x16x32_bf16 v[130:133], v[224:227], v[184:187], v[130:133]
	v_mfma_f32_16x16x32_bf16 v[118:121], v[216:219], v[192:195], v[118:121]
	v_mfma_f32_16x16x32_bf16 v[114:117], v[224:227], v[192:195], v[114:117]
	v_mfma_f32_16x16x32_bf16 v[102:105], v[216:219], v[200:203], v[102:105]
	v_mfma_f32_16x16x32_bf16 v[98:101], v[224:227], v[200:203], v[98:101]
	v_mfma_f32_16x16x32_bf16 v[86:89], v[216:219], v[208:211], v[86:89]
	v_mfma_f32_16x16x32_bf16 v[82:85], v[224:227], v[208:211], v[82:85]
	v_mfma_f32_16x16x32_bf16 v[134:137], v[220:223], v[188:191], v[134:137]
	v_mfma_f32_16x16x32_bf16 v[130:133], v[228:231], v[188:191], v[130:133]
	v_mfma_f32_16x16x32_bf16 v[118:121], v[220:223], v[196:199], v[118:121]
	v_mfma_f32_16x16x32_bf16 v[114:117], v[228:231], v[196:199], v[114:117]
	v_mfma_f32_16x16x32_bf16 v[102:105], v[220:223], v[204:207], v[102:105]
	v_mfma_f32_16x16x32_bf16 v[98:101], v[228:231], v[204:207], v[98:101]
	v_mfma_f32_16x16x32_bf16 v[86:89], v[220:223], v[212:215], v[86:89]
	v_mfma_f32_16x16x32_bf16 v[82:85], v[228:231], v[212:215], v[82:85]
	s_setprio 0
	s_mov_b32 m0, s50
	v_lshl_add_u64 v[162:163], v[234:235], 0, s[10:11]
	s_barrier
	ds_read_b128 v[184:187], v165 offset:49152
	ds_read_b128 v[188:191], v165 offset:50176
	ds_read_b128 v[192:195], v165 offset:51200
	ds_read_b128 v[196:199], v165 offset:52224
	ds_read_b128 v[200:203], v165 offset:53248
	ds_read_b128 v[204:207], v165 offset:54272
	ds_read_b128 v[208:211], v165 offset:55296
	ds_read_b128 v[212:215], v165 offset:56320
	global_load_lds_dwordx4 v[162:163], off
	v_lshl_add_u64 v[162:163], v[236:237], 0, s[10:11]
	s_mov_b32 m0, s51
	s_nop 0
	global_load_lds_dwordx4 v[162:163], off
	s_barrier
	s_waitcnt lgkmcnt(0)
	s_setprio 1
	s_waitcnt lgkmcnt(0)
	v_mfma_f32_16x16x32_bf16 v[78:81], v[168:171], v[184:187], v[78:81]
	v_mfma_f32_16x16x32_bf16 v[74:77], v[176:179], v[184:187], v[74:77]
	v_mfma_f32_16x16x32_bf16 v[66:69], v[168:171], v[192:195], v[66:69]
	v_mfma_f32_16x16x32_bf16 v[58:61], v[176:179], v[192:195], v[58:61]
	v_mfma_f32_16x16x32_bf16 v[50:53], v[168:171], v[200:203], v[50:53]
	v_mfma_f32_16x16x32_bf16 v[42:45], v[176:179], v[200:203], v[42:45]
	v_mfma_f32_16x16x32_bf16 v[34:37], v[168:171], v[208:211], v[34:37]
	v_mfma_f32_16x16x32_bf16 v[26:29], v[176:179], v[208:211], v[26:29]
	v_mfma_f32_16x16x32_bf16 v[78:81], v[172:175], v[188:191], v[78:81]
	v_mfma_f32_16x16x32_bf16 v[74:77], v[180:183], v[188:191], v[74:77]
	v_mfma_f32_16x16x32_bf16 v[66:69], v[172:175], v[196:199], v[66:69]
	v_mfma_f32_16x16x32_bf16 v[58:61], v[180:183], v[196:199], v[58:61]
	v_mfma_f32_16x16x32_bf16 v[50:53], v[172:175], v[204:207], v[50:53]
	v_mfma_f32_16x16x32_bf16 v[42:45], v[180:183], v[204:207], v[42:45]
	v_mfma_f32_16x16x32_bf16 v[34:37], v[172:175], v[212:215], v[34:37]
	v_mfma_f32_16x16x32_bf16 v[26:29], v[180:183], v[212:215], v[26:29]
	s_setprio 0
	s_barrier
	s_add_u32 s30, s30, 0x80080
	s_addc_u32 s31, s31, 0
	s_add_i32 s34, s34, s44
	v_lshl_add_u64 v[162:163], s[30:31], 0, v[148:149]
	s_mov_b32 m0, s34
	s_nop 0
	global_load_lds_dwordx4 v[162:163], off
	v_lshl_add_u64 v[162:163], s[30:31], 0, v[152:153]
	s_add_i32 m0, s34, 0x2000
	s_nop 0
	global_load_lds_dwordx4 v[162:163], off
	s_waitcnt vmcnt(6)
	s_barrier
	s_setprio 1
	v_mfma_f32_16x16x32_bf16 v[70:73], v[216:219], v[184:187], v[70:73]
	v_mfma_f32_16x16x32_bf16 v[62:65], v[224:227], v[184:187], v[62:65]
	v_mfma_f32_16x16x32_bf16 v[54:57], v[216:219], v[192:195], v[54:57]
	v_mfma_f32_16x16x32_bf16 v[46:49], v[224:227], v[192:195], v[46:49]
	v_mfma_f32_16x16x32_bf16 v[38:41], v[216:219], v[200:203], v[38:41]
	v_mfma_f32_16x16x32_bf16 v[30:33], v[224:227], v[200:203], v[30:33]
	v_mfma_f32_16x16x32_bf16 v[22:25], v[216:219], v[208:211], v[22:25]
	v_mfma_f32_16x16x32_bf16 v[18:21], v[224:227], v[208:211], v[18:21]
	v_mfma_f32_16x16x32_bf16 v[70:73], v[220:223], v[188:191], v[70:73]
	v_mfma_f32_16x16x32_bf16 v[62:65], v[228:231], v[188:191], v[62:65]
	v_mfma_f32_16x16x32_bf16 v[54:57], v[220:223], v[196:199], v[54:57]
	v_mfma_f32_16x16x32_bf16 v[46:49], v[228:231], v[196:199], v[46:49]
	v_mfma_f32_16x16x32_bf16 v[38:41], v[220:223], v[204:207], v[38:41]
	v_mfma_f32_16x16x32_bf16 v[30:33], v[228:231], v[204:207], v[30:33]
	v_mfma_f32_16x16x32_bf16 v[22:25], v[220:223], v[212:215], v[22:25]
	v_mfma_f32_16x16x32_bf16 v[18:21], v[228:231], v[212:215], v[18:21]
	s_setprio 0
	s_add_i32 s64, s64, 2
	s_add_u32 s28, s28, 0x100
	s_addc_u32 s29, s29, 0
	s_add_u32 s62, s62, 0x100
	s_addc_u32 s63, s63, 0
	s_cmp_gt_u32 s64, 29
	s_barrier
	s_cbranch_scc0 .LBB0_1106
	v_mov_b32_e32 v162, v0
	s_lshl_b32 s6, s6, 8
	v_readfirstlane_b32 s7, v162
	s_ashr_i32 s21, s7, 2
	s_andn2_b32 s21, s21, 63
	s_add_i32 s21, s21, s6
	s_lshr_b32 s7, s7, 1
	v_and_or_b32 v168, v162, 15, s21
	s_lshl_b32 s6, s59, 8
	s_and_b32 s21, s7, 0x60
	v_lshrrev_b32_e32 v162, 1, v162
	s_or_b32 s6, s21, s6
	v_and_b32_e32 v167, 24, v162
	v_or_b32_e32 v162, s6, v167
	v_ashrrev_i32_e32 v169, 31, v168
	v_ashrrev_i32_e32 v163, 31, v162
	v_lshlrev_b64 v[170:171], 13, v[168:169]
	v_lshl_add_u64 v[170:171], s[8:9], 0, v[170:171]
	v_lshlrev_b64 v[172:173], 1, v[162:163]
	s_waitcnt vmcnt(6)
	v_lshl_add_u64 v[162:163], v[170:171], 0, v[172:173]
	v_pk_mul_f32 v[144:145], v[144:145], v[12:13]
	v_pk_mul_f32 v[142:143], v[142:143], v[10:11]
	v_pk_mul_f32 v[170:171], v[140:141], v[16:17]
	v_pk_mul_f32 v[140:141], v[138:139], v[14:15]
	v_cvt_pk_bf16_f32 v138, v142, v143
	v_cvt_pk_bf16_f32 v139, v144, v145
	v_pk_mul_f32 v[134:135], v[134:135], v[2:3]
	v_cvt_pk_bf16_f32 v140, v140, v141
	v_cvt_pk_bf16_f32 v141, v170, v171
	global_store_dwordx4 v[162:163], v[138:141], off
	v_pk_mul_f32 v[136:137], v[136:137], v[4:5]
	v_pk_mul_f32 v[128:129], v[128:129], v[12:13]
	v_pk_mul_f32 v[138:139], v[132:133], v[8:9]
	v_pk_mul_f32 v[132:133], v[130:131], v[6:7]
	v_cvt_pk_bf16_f32 v130, v134, v135
	v_cvt_pk_bf16_f32 v131, v136, v137
	v_pk_mul_f32 v[126:127], v[126:127], v[10:11]
	v_cvt_pk_bf16_f32 v132, v132, v133
	v_cvt_pk_bf16_f32 v133, v138, v139
	global_store_dwordx4 v[162:163], v[130:133], off offset:256
	v_pk_mul_f32 v[118:119], v[118:119], v[2:3]
	v_pk_mul_f32 v[120:121], v[120:121], v[4:5]
	v_or_b32_e32 v130, 16, v168
	v_ashrrev_i32_e32 v131, 31, v130
	v_lshlrev_b64 v[130:131], 13, v[130:131]
	v_lshl_add_u64 v[130:131], s[8:9], 0, v[130:131]
	v_lshl_add_u64 v[130:131], v[130:131], 0, v[172:173]
	v_pk_mul_f32 v[132:133], v[124:125], v[16:17]
	v_pk_mul_f32 v[124:125], v[122:123], v[14:15]
	v_cvt_pk_bf16_f32 v122, v126, v127
	v_cvt_pk_bf16_f32 v123, v128, v129
	v_pk_mul_f32 v[112:113], v[112:113], v[12:13]
	v_cvt_pk_bf16_f32 v124, v124, v125
	v_cvt_pk_bf16_f32 v125, v132, v133
	global_store_dwordx4 v[130:131], v[122:125], off
	v_pk_mul_f32 v[110:111], v[110:111], v[10:11]
	v_pk_mul_f32 v[102:103], v[102:103], v[2:3]
	v_pk_mul_f32 v[122:123], v[116:117], v[8:9]
	v_pk_mul_f32 v[116:117], v[114:115], v[6:7]
	v_cvt_pk_bf16_f32 v114, v118, v119
	v_cvt_pk_bf16_f32 v115, v120, v121
	v_pk_mul_f32 v[104:105], v[104:105], v[4:5]
	v_cvt_pk_bf16_f32 v116, v116, v117
	v_cvt_pk_bf16_f32 v117, v122, v123
	global_store_dwordx4 v[130:131], v[114:117], off offset:256
	v_pk_mul_f32 v[96:97], v[96:97], v[12:13]
	v_pk_mul_f32 v[94:95], v[94:95], v[10:11]
	v_or_b32_e32 v114, 32, v168
	v_ashrrev_i32_e32 v115, 31, v114
	v_lshlrev_b64 v[114:115], 13, v[114:115]
	v_lshl_add_u64 v[114:115], s[8:9], 0, v[114:115]
	v_lshl_add_u64 v[114:115], v[114:115], 0, v[172:173]
	v_pk_mul_f32 v[116:117], v[108:109], v[16:17]
	v_pk_mul_f32 v[108:109], v[106:107], v[14:15]
	v_cvt_pk_bf16_f32 v106, v110, v111
	v_cvt_pk_bf16_f32 v107, v112, v113
	v_pk_mul_f32 v[88:89], v[88:89], v[4:5]
	v_cvt_pk_bf16_f32 v108, v108, v109
	v_cvt_pk_bf16_f32 v109, v116, v117
	global_store_dwordx4 v[114:115], v[106:109], off
	v_pk_mul_f32 v[86:87], v[86:87], v[2:3]
	v_pk_mul_f32 v[78:79], v[78:79], v[10:11]
	v_pk_mul_f32 v[106:107], v[100:101], v[8:9]
	v_pk_mul_f32 v[100:101], v[98:99], v[6:7]
	v_cvt_pk_bf16_f32 v98, v102, v103
	v_cvt_pk_bf16_f32 v99, v104, v105
	v_pk_mul_f32 v[80:81], v[80:81], v[12:13]
	v_cvt_pk_bf16_f32 v100, v100, v101
	v_cvt_pk_bf16_f32 v101, v106, v107
	global_store_dwordx4 v[114:115], v[98:101], off offset:256
	v_pk_mul_f32 v[72:73], v[72:73], v[4:5]
	v_pk_mul_f32 v[70:71], v[70:71], v[2:3]
	v_or_b32_e32 v98, 48, v168
	v_ashrrev_i32_e32 v99, 31, v98
	v_lshlrev_b64 v[98:99], 13, v[98:99]
	v_lshl_add_u64 v[98:99], s[8:9], 0, v[98:99]
	v_lshl_add_u64 v[98:99], v[98:99], 0, v[172:173]
	v_pk_mul_f32 v[100:101], v[92:93], v[16:17]
	v_pk_mul_f32 v[92:93], v[90:91], v[14:15]
	v_cvt_pk_bf16_f32 v90, v94, v95
	v_cvt_pk_bf16_f32 v91, v96, v97
	v_pk_mul_f32 v[66:67], v[66:67], v[10:11]
	v_cvt_pk_bf16_f32 v92, v92, v93
	v_cvt_pk_bf16_f32 v93, v100, v101
	global_store_dwordx4 v[98:99], v[90:93], off
	v_pk_mul_f32 v[56:57], v[56:57], v[4:5]
	v_pk_mul_f32 v[54:55], v[54:55], v[2:3]
	v_pk_mul_f32 v[90:91], v[84:85], v[8:9]
	v_pk_mul_f32 v[84:85], v[82:83], v[6:7]
	v_readfirstlane_b32 s99, v0
	s_cmpk_gt_u32 s99, 0xff
	s_cbranch_scc1 .Lz0_1106
	s_barrier
.Lz0_1106:
	v_cvt_pk_bf16_f32 v82, v86, v87
	v_cvt_pk_bf16_f32 v83, v88, v89
	v_pk_mul_f32 v[50:51], v[50:51], v[10:11]
	v_cvt_pk_bf16_f32 v84, v84, v85
	v_cvt_pk_bf16_f32 v85, v90, v91
	global_store_dwordx4 v[98:99], v[82:85], off offset:256
	v_pk_mul_f32 v[10:11], v[34:35], v[10:11]
	v_pk_mul_f32 v[40:41], v[40:41], v[4:5]
	v_pk_mul_f32 v[84:85], v[76:77], v[16:17]
	v_pk_mul_f32 v[76:77], v[74:75], v[14:15]
	v_cvt_pk_bf16_f32 v74, v78, v79
	v_add_co_u32_e64 v78, s[6:7], s55, v162
	v_cvt_pk_bf16_f32 v75, v80, v81
	v_cvt_pk_bf16_f32 v76, v76, v77
	v_cvt_pk_bf16_f32 v77, v84, v85
	v_lshl_add_u64 v[82:83], v[162:163], 0, s[12:13]
	s_nop 0
	v_addc_co_u32_e64 v79, s[6:7], 0, v163, s[6:7]
	global_store_dwordx4 v[78:79], v[74:77], off
	v_pk_mul_f32 v[38:39], v[38:39], v[2:3]
	v_pk_mul_f32 v[4:5], v[24:25], v[4:5]
	v_pk_mul_f32 v[74:75], v[64:65], v[8:9]
	v_pk_mul_f32 v[64:65], v[62:63], v[6:7]
	v_cvt_pk_bf16_f32 v62, v70, v71
	v_cvt_pk_bf16_f32 v63, v72, v73
	v_pk_mul_f32 v[2:3], v[22:23], v[2:3]
	v_cvt_pk_bf16_f32 v64, v64, v65
	v_cvt_pk_bf16_f32 v65, v74, v75
	global_store_dwordx4 v[82:83], v[62:65], off offset:256
	s_and_b64 vcc, vcc, exec
	v_readlane_b32 s72, v254, 51
	v_pk_mul_f32 v[64:65], v[68:69], v[12:13]
	v_pk_mul_f32 v[68:69], v[60:61], v[16:17]
	v_pk_mul_f32 v[60:61], v[58:59], v[14:15]
	v_cvt_pk_bf16_f32 v58, v66, v67
	v_cvt_pk_bf16_f32 v59, v64, v65
	v_add_co_u32_e64 v64, s[6:7], s56, v162
	v_cvt_pk_bf16_f32 v60, v60, v61
	v_cvt_pk_bf16_f32 v61, v68, v69
	v_lshl_add_u64 v[62:63], v[162:163], 0, s[14:15]
	s_nop 0
	v_addc_co_u32_e64 v65, s[6:7], 0, v163, s[6:7]
	global_store_dwordx4 v[64:65], v[58:61], off
	v_readlane_b32 s73, v254, 52
	s_nop 0
	v_pk_mul_f32 v[58:59], v[48:49], v[8:9]
	v_pk_mul_f32 v[48:49], v[46:47], v[6:7]
	v_cvt_pk_bf16_f32 v46, v54, v55
	v_cvt_pk_bf16_f32 v47, v56, v57
	s_nop 0
	v_cvt_pk_bf16_f32 v48, v48, v49
	v_cvt_pk_bf16_f32 v49, v58, v59
	global_store_dwordx4 v[62:63], v[46:49], off offset:256
	s_nop 1
	v_pk_mul_f32 v[48:49], v[52:53], v[12:13]
	v_pk_mul_f32 v[52:53], v[44:45], v[16:17]
	v_pk_mul_f32 v[44:45], v[42:43], v[14:15]
	v_cvt_pk_bf16_f32 v42, v50, v51
	v_cvt_pk_bf16_f32 v43, v48, v49
	v_add_co_u32_e64 v48, s[6:7], s57, v162
	v_lshl_add_u64 v[46:47], v[162:163], 0, s[16:17]
	s_nop 0
	v_addc_co_u32_e64 v49, s[6:7], 0, v163, s[6:7]
	v_cvt_pk_bf16_f32 v44, v44, v45
	v_cvt_pk_bf16_f32 v45, v52, v53
	global_store_dwordx4 v[48:49], v[42:45], off
	v_pk_mul_f32 v[12:13], v[36:37], v[12:13]
	v_pk_mul_f32 v[14:15], v[26:27], v[14:15]
	v_pk_mul_f32 v[42:43], v[32:33], v[8:9]
	v_pk_mul_f32 v[32:33], v[30:31], v[6:7]
	v_cvt_pk_bf16_f32 v30, v38, v39
	v_cvt_pk_bf16_f32 v31, v40, v41
	v_pk_mul_f32 v[16:17], v[28:29], v[16:17]
	v_cvt_pk_bf16_f32 v32, v32, v33
	v_cvt_pk_bf16_f32 v33, v42, v43
	global_store_dwordx4 v[46:47], v[30:33], off offset:256
	v_cvt_pk_bf16_f32 v10, v10, v11
	v_cvt_pk_bf16_f32 v11, v12, v13
	v_cvt_pk_bf16_f32 v12, v14, v15
	v_add_co_u32_e64 v14, s[6:7], s58, v162
	s_nop 0
	v_lshl_add_u64 v[30:31], v[162:163], 0, s[18:19]
	v_addc_co_u32_e64 v15, s[6:7], 0, v163, s[6:7]
	v_cvt_pk_bf16_f32 v13, v16, v17
	global_store_dwordx4 v[14:15], v[10:13], off
	v_pk_mul_f32 v[8:9], v[20:21], v[8:9]
	v_pk_mul_f32 v[6:7], v[18:19], v[6:7]
	v_cvt_pk_bf16_f32 v2, v2, v3
	v_cvt_pk_bf16_f32 v3, v4, v5
	s_mov_b64 s[6:7], -1
	v_cvt_pk_bf16_f32 v4, v6, v7
	v_cvt_pk_bf16_f32 v5, v8, v9
	global_store_dwordx4 v[30:31], v[2:5], off offset:256
	v_readfirstlane_b32 s99, v0
	s_cmpk_gt_u32 s99, 0xff
	s_cbranch_scc0 .Lz1_1106
	s_barrier

.LBB0_1442:
	s_add_u32 s48, s96, s46
	s_addc_u32 s49, s97, s47
	s_add_u32 s50, s48, 0x32370200
	ds_read_b128 v[188:191], v176
	ds_read_b128 v[192:195], v176 offset:1024
	ds_read_b128 v[196:199], v176 offset:2048
	ds_read_b128 v[200:203], v176 offset:3072
	s_addc_u32 s51, s49, 0
	s_add_u32 s81, s78, s46
	s_addc_u32 s82, s79, s47
	s_cmpk_eq_i32 s46, 0x600
	s_cselect_b64 vcc, -1, 0
	s_and_b64 s[48:49], vcc, exec
	v_cndmask_b32_e32 v166, v184, v180, vcc
	s_cselect_b32 s51, s11, s51
	s_cselect_b32 s50, s10, s50
	v_cndmask_b32_e32 v252, v172, v182, vcc
	v_cndmask_b32_e32 v169, v168, v181, vcc
	v_cndmask_b32_e32 v171, v170, v183, vcc
	s_cselect_b32 s49, s39, s82
	s_cselect_b32 s48, s41, s81
	s_mov_b32 m0, s45
	v_lshl_add_u64 v[6:7], v[4:5], 0, s[46:47]
	ds_read_b128 v[10:13], v177
	ds_read_b128 v[14:17], v177 offset:1024
	ds_read_b128 v[204:207], v177 offset:2048
	ds_read_b128 v[208:211], v177 offset:3072
	ds_read_b128 v[212:215], v177 offset:4096
	ds_read_b128 v[216:219], v177 offset:5120
	ds_read_b128 v[220:223], v177 offset:6144
	ds_read_b128 v[224:227], v177 offset:7168
	global_load_lds_dwordx4 v[6:7], off
	v_lshl_add_u64 v[6:7], v[2:3], 0, s[46:47]
	s_mov_b32 m0, s69
	s_nop 0
	global_load_lds_dwordx4 v[6:7], off
	ds_read_b128 v[228:231], v178
	ds_read_b128 v[232:235], v178 offset:1024
	ds_read_b128 v[236:239], v178 offset:2048
	ds_read_b128 v[240:243], v178 offset:3072
	s_waitcnt vmcnt(8) lgkmcnt(0)
	s_barrier
	s_setprio 1
	v_mfma_f32_16x16x128_f8f6f4 v[154:157], v[188:195], v[10:17], v[154:157]
	v_mfma_f32_16x16x128_f8f6f4 v[146:149], v[196:203], v[10:17], v[146:149]
	v_mfma_f32_16x16x128_f8f6f4 v[138:141], v[188:195], v[204:211], v[138:141]
	v_mfma_f32_16x16x128_f8f6f4 v[130:133], v[196:203], v[204:211], v[130:133]
	v_mfma_f32_16x16x128_f8f6f4 v[122:125], v[188:195], v[212:219], v[122:125]
	v_mfma_f32_16x16x128_f8f6f4 v[114:117], v[196:203], v[212:219], v[114:117]
	v_mfma_f32_16x16x128_f8f6f4 v[106:109], v[188:195], v[220:227], v[106:109]
	v_mfma_f32_16x16x128_f8f6f4 v[90:93], v[196:203], v[220:227], v[90:93]
	v_mfma_f32_16x16x128_f8f6f4 v[158:161], v[228:235], v[10:17], v[158:161]
	v_mfma_f32_16x16x128_f8f6f4 v[150:153], v[236:243], v[10:17], v[150:153]
	v_mfma_f32_16x16x128_f8f6f4 v[142:145], v[228:235], v[204:211], v[142:145]
	v_mfma_f32_16x16x128_f8f6f4 v[134:137], v[236:243], v[204:211], v[134:137]
	v_mfma_f32_16x16x128_f8f6f4 v[126:129], v[228:235], v[212:219], v[126:129]
	v_mfma_f32_16x16x128_f8f6f4 v[118:121], v[236:243], v[212:219], v[118:121]
	v_mfma_f32_16x16x128_f8f6f4 v[110:113], v[228:235], v[220:227], v[110:113]
	v_mfma_f32_16x16x128_f8f6f4 v[98:101], v[236:243], v[220:227], v[98:101]
	s_setprio 0
	s_barrier
	ds_read_b128 v[204:207], v177 offset:16384
	ds_read_b128 v[208:211], v177 offset:17408
	ds_read_b128 v[212:215], v177 offset:18432
	ds_read_b128 v[216:219], v177 offset:19456
	ds_read_b128 v[220:223], v177 offset:20480
	ds_read_b128 v[224:227], v177 offset:21504
	ds_read_b128 v[244:247], v177 offset:22528
	ds_read_b128 v[248:251], v177 offset:23552
	s_mov_b32 m0, s70
	v_lshl_add_u64 v[6:7], s[48:49], 0, v[162:163]
	global_load_lds_dwordx4 v[6:7], off
	v_lshl_add_u64 v[8:9], s[48:49], 0, v[164:165]
	s_mov_b32 m0, s71
	s_nop 0
	global_load_lds_dwordx4 v[8:9], off
	s_mov_b32 m0, s55
	s_nop 0
	global_load_lds_dwordx4 v166, s[50:51]
	s_mov_b32 m0, s56
	v_mov_b32_e32 v253, v167
	global_load_lds_dwordx4 v252, s[50:51]
	s_add_u32 s82, s48, 0x40000
	s_addc_u32 s83, s49, 0
	s_mov_b32 m0, s72
	v_lshl_add_u64 v[14:15], s[82:83], 0, v[162:163]
	global_load_lds_dwordx4 v[14:15], off
	v_lshl_add_u64 v[14:15], s[82:83], 0, v[164:165]
	s_mov_b32 m0, s73
	s_nop 0
	global_load_lds_dwordx4 v[14:15], off
	s_waitcnt vmcnt(8) lgkmcnt(0)
	s_barrier
	v_lshl_add_u64 v[12:13], s[50:51], 0, v[166:167]
	v_lshl_add_u64 v[10:11], s[50:51], 0, v[252:253]
	s_setprio 1
	v_mfma_f32_16x16x128_f8f6f4 v[94:97], v[188:195], v[204:211], v[94:97]
	v_mfma_f32_16x16x128_f8f6f4 v[82:85], v[196:203], v[204:211], v[82:85]
	v_mfma_f32_16x16x128_f8f6f4 v[74:77], v[188:195], v[212:219], v[74:77]
	v_mfma_f32_16x16x128_f8f6f4 v[66:69], v[196:203], v[212:219], v[66:69]
	v_mfma_f32_16x16x128_f8f6f4 v[58:61], v[188:195], v[220:227], v[58:61]
	v_mfma_f32_16x16x128_f8f6f4 v[50:53], v[196:203], v[220:227], v[50:53]
	v_mfma_f32_16x16x128_f8f6f4 v[42:45], v[188:195], v[244:251], v[42:45]
	v_mfma_f32_16x16x128_f8f6f4 v[34:37], v[196:203], v[244:251], v[34:37]
	v_mfma_f32_16x16x128_f8f6f4 v[102:105], v[228:235], v[204:211], v[102:105]
	v_mfma_f32_16x16x128_f8f6f4 v[86:89], v[236:243], v[204:211], v[86:89]
	v_mfma_f32_16x16x128_f8f6f4 v[78:81], v[228:235], v[212:219], v[78:81]
	v_mfma_f32_16x16x128_f8f6f4 v[70:73], v[236:243], v[212:219], v[70:73]
	v_mfma_f32_16x16x128_f8f6f4 v[62:65], v[228:235], v[220:227], v[62:65]
	v_mfma_f32_16x16x128_f8f6f4 v[54:57], v[236:243], v[220:227], v[54:57]
	v_mfma_f32_16x16x128_f8f6f4 v[46:49], v[228:235], v[244:251], v[46:49]
	v_mfma_f32_16x16x128_f8f6f4 v[38:41], v[236:243], v[244:251], v[38:41]
	s_setprio 0
	s_barrier
	ds_read_b128 v[188:191], v185
	ds_read_b128 v[192:195], v185 offset:1024
	ds_read_b128 v[196:199], v185 offset:2048
	ds_read_b128 v[200:203], v185 offset:3072
	s_mov_b32 m0, s57
	ds_read_b128 v[204:207], v177 offset:32768
	ds_read_b128 v[208:211], v177 offset:33792
	ds_read_b128 v[212:215], v177 offset:34816
	ds_read_b128 v[216:219], v177 offset:35840
	ds_read_b128 v[220:223], v177 offset:36864
	ds_read_b128 v[224:227], v177 offset:37888
	ds_read_b128 v[228:231], v177 offset:38912
	ds_read_b128 v[232:235], v177 offset:39936
	global_load_lds_dwordx4 v169, s[50:51]
	s_mov_b32 m0, s58
	s_nop 0
	global_load_lds_dwordx4 v171, s[50:51]
	ds_read_b128 v[236:239], v186
	ds_read_b128 v[240:243], v186 offset:1024
	ds_read_b128 v[244:247], v186 offset:2048
	ds_read_b128 v[248:251], v186 offset:3072
	s_waitcnt vmcnt(8) lgkmcnt(0)
	s_barrier
	s_setprio 1
	v_mfma_f32_16x16x128_f8f6f4 v[154:157], v[188:195], v[204:211], v[154:157]
	v_mfma_f32_16x16x128_f8f6f4 v[146:149], v[196:203], v[204:211], v[146:149]
	v_mfma_f32_16x16x128_f8f6f4 v[138:141], v[188:195], v[212:219], v[138:141]
	v_mfma_f32_16x16x128_f8f6f4 v[130:133], v[196:203], v[212:219], v[130:133]
	v_mfma_f32_16x16x128_f8f6f4 v[122:125], v[188:195], v[220:227], v[122:125]
	v_mfma_f32_16x16x128_f8f6f4 v[114:117], v[196:203], v[220:227], v[114:117]
	v_mfma_f32_16x16x128_f8f6f4 v[106:109], v[188:195], v[228:235], v[106:109]
	v_mfma_f32_16x16x128_f8f6f4 v[90:93], v[196:203], v[228:235], v[90:93]
	v_mfma_f32_16x16x128_f8f6f4 v[158:161], v[236:243], v[204:211], v[158:161]
	v_mfma_f32_16x16x128_f8f6f4 v[150:153], v[244:251], v[204:211], v[150:153]
	v_mfma_f32_16x16x128_f8f6f4 v[142:145], v[236:243], v[212:219], v[142:145]
	v_mfma_f32_16x16x128_f8f6f4 v[134:137], v[244:251], v[212:219], v[134:137]
	v_mfma_f32_16x16x128_f8f6f4 v[126:129], v[236:243], v[220:227], v[126:129]
	v_mfma_f32_16x16x128_f8f6f4 v[118:121], v[244:251], v[220:227], v[118:121]
	v_mfma_f32_16x16x128_f8f6f4 v[110:113], v[236:243], v[228:235], v[110:113]
	v_mfma_f32_16x16x128_f8f6f4 v[98:101], v[244:251], v[228:235], v[98:101]
	s_setprio 0
	s_barrier
	ds_read_b128 v[204:207], v177 offset:49152
	ds_read_b128 v[208:211], v177 offset:50176
	ds_read_b128 v[212:215], v177 offset:51200
	ds_read_b128 v[216:219], v177 offset:52224
	ds_read_b128 v[220:223], v177 offset:53248
	ds_read_b128 v[224:227], v177 offset:54272
	ds_read_b128 v[228:231], v177 offset:55296
	ds_read_b128 v[232:235], v177 offset:56320
	s_mov_b32 m0, s74
	v_lshl_add_u64 v[6:7], v[6:7], 0, s[18:19]
	global_load_lds_dwordx4 v[6:7], off
	v_lshl_add_u64 v[6:7], v[8:9], 0, s[18:19]
	s_mov_b32 m0, s75
	s_nop 0
	global_load_lds_dwordx4 v[6:7], off
	s_mov_b32 m0, s60
	v_lshl_add_u64 v[6:7], v[12:13], 0, s[18:19]
	global_load_lds_dwordx4 v[6:7], off
	v_lshl_add_u64 v[6:7], v[10:11], 0, s[18:19]
	s_mov_b32 m0, s61
	s_nop 0
	global_load_lds_dwordx4 v[6:7], off
	s_add_u32 s48, s48, 0x40080
	s_addc_u32 s49, s49, 0
	s_mov_b32 m0, s76
	v_lshl_add_u64 v[6:7], s[48:49], 0, v[162:163]
	global_load_lds_dwordx4 v[6:7], off
	v_lshl_add_u64 v[6:7], s[48:49], 0, v[164:165]
	s_mov_b32 m0, s77
	s_nop 0
	global_load_lds_dwordx4 v[6:7], off
	s_waitcnt vmcnt(8) lgkmcnt(0)
	s_barrier
	s_setprio 1
	v_mfma_f32_16x16x128_f8f6f4 v[94:97], v[188:195], v[204:211], v[94:97]
	v_mfma_f32_16x16x128_f8f6f4 v[82:85], v[196:203], v[204:211], v[82:85]
	v_mfma_f32_16x16x128_f8f6f4 v[74:77], v[188:195], v[212:219], v[74:77]
	v_mfma_f32_16x16x128_f8f6f4 v[66:69], v[196:203], v[212:219], v[66:69]
	v_mfma_f32_16x16x128_f8f6f4 v[58:61], v[188:195], v[220:227], v[58:61]
	v_mfma_f32_16x16x128_f8f6f4 v[50:53], v[196:203], v[220:227], v[50:53]
	v_mfma_f32_16x16x128_f8f6f4 v[42:45], v[188:195], v[228:235], v[42:45]
	v_mfma_f32_16x16x128_f8f6f4 v[34:37], v[196:203], v[228:235], v[34:37]
	v_mfma_f32_16x16x128_f8f6f4 v[102:105], v[236:243], v[204:211], v[102:105]
	v_mfma_f32_16x16x128_f8f6f4 v[86:89], v[244:251], v[204:211], v[86:89]
	v_mfma_f32_16x16x128_f8f6f4 v[78:81], v[236:243], v[212:219], v[78:81]
	v_mfma_f32_16x16x128_f8f6f4 v[70:73], v[244:251], v[212:219], v[70:73]
	v_mfma_f32_16x16x128_f8f6f4 v[62:65], v[236:243], v[220:227], v[62:65]
	v_mfma_f32_16x16x128_f8f6f4 v[54:57], v[244:251], v[220:227], v[54:57]
	v_mfma_f32_16x16x128_f8f6f4 v[46:49], v[236:243], v[228:235], v[46:49]
	v_mfma_f32_16x16x128_f8f6f4 v[38:41], v[244:251], v[228:235], v[38:41]
	s_setprio 0
	s_add_i32 s80, s80, 2
	s_add_u32 s46, s46, 0x100
	s_addc_u32 s47, s47, 0
	s_cmp_gt_u32 s80, 13
	s_barrier
	s_cbranch_scc0 .LBB0_1442
	v_mov_b32_e32 v2, v0
	s_nop 15
	s_nop 15
	s_waitcnt vmcnt(6)
	s_lshl_b32 s41, s68, 8
	v_readfirstlane_b32 s39, v2
	v_pk_fma_f32 v[10:11], v[154:155], s[30:31], v[30:31] op_sel_hi:[1,0,1]
	s_ashr_i32 s45, s39, 2
	v_min_f32_e32 v10, 0x40e00000, v10
	v_min_f32_e32 v11, 0x40e00000, v11
	s_andn2_b32 s45, s45, 63
	v_pk_mul_f32 v[12:13], v[10:11], s[34:35] op_sel_hi:[1,0]
	s_add_i32 s45, s45, s41
	v_exp_f32_e32 v12, v12
	v_exp_f32_e32 v13, v13
	v_and_or_b32 v6, v2, 15, s45
	v_lshrrev_b32_e32 v2, 1, v2
	v_and_b32_e32 v8, 24, v2
	v_pk_fma_f32 v[2:3], v[156:157], s[30:31], v[32:33] op_sel_hi:[1,0,1]
	v_pk_add_f32 v[12:13], v[12:13], 1.0 op_sel_hi:[1,0]
	v_min_f32_e32 v2, 0x40e00000, v2
	v_min_f32_e32 v3, 0x40e00000, v3
	v_pk_mul_f32 v[154:155], v[2:3], s[34:35] op_sel_hi:[1,0]
	v_rcp_f32_e32 v12, v12
	v_rcp_f32_e32 v13, v13
	v_exp_f32_e32 v154, v154
	v_exp_f32_e32 v155, v155
	v_pk_fma_f32 v[16:17], v[158:159], s[30:31], v[26:27] op_sel_hi:[1,0,1]
	v_pk_fma_f32 v[14:15], v[160:161], s[30:31], v[28:29] op_sel_hi:[1,0,1]
	v_med3_f32 v16, v16, s65, v179
	v_med3_f32 v17, v17, s65, v179
	v_pk_fma_f32 v[10:11], v[16:17], v[10:11], v[10:11]
	v_med3_f32 v14, v14, s65, v179
	v_med3_f32 v15, v15, s65, v179
	v_pk_mul_f32 v[10:11], v[10:11], v[12:13]
	v_pk_add_f32 v[12:13], v[154:155], 1.0 op_sel_hi:[1,0]
	v_pk_fma_f32 v[2:3], v[14:15], v[2:3], v[2:3]
	v_pk_fma_f32 v[14:15], v[146:147], s[30:31], v[22:23] op_sel_hi:[1,0,1]
	v_rcp_f32_e32 v12, v12
	v_rcp_f32_e32 v13, v13
	v_min_f32_e32 v14, 0x40e00000, v14
	v_min_f32_e32 v15, 0x40e00000, v15
	v_pk_mul_f32 v[146:147], v[14:15], s[34:35] op_sel_hi:[1,0]
	v_pk_mul_f32 v[2:3], v[2:3], v[12:13]
	v_exp_f32_e32 v146, v146
	v_exp_f32_e32 v147, v147
	v_pk_fma_f32 v[12:13], v[148:149], s[30:31], v[24:25] op_sel_hi:[1,0,1]
	v_pk_fma_f32 v[148:149], v[150:151], s[30:31], v[18:19] op_sel_hi:[1,0,1]
	v_min_f32_e32 v12, 0x40e00000, v12
	v_med3_f32 v148, v148, s65, v179
	v_med3_f32 v149, v149, s65, v179
	v_min_f32_e32 v13, 0x40e00000, v13
	v_pk_add_f32 v[146:147], v[146:147], 1.0 op_sel_hi:[1,0]
	v_pk_fma_f32 v[14:15], v[148:149], v[14:15], v[14:15]
	v_pk_mul_f32 v[148:149], v[12:13], s[34:35] op_sel_hi:[1,0]
	v_rcp_f32_e32 v146, v146
	v_rcp_f32_e32 v147, v147
	v_exp_f32_e32 v148, v148
	v_exp_f32_e32 v149, v149
	v_pk_fma_f32 v[16:17], v[152:153], s[30:31], v[20:21] op_sel_hi:[1,0,1]
	v_pk_mul_f32 v[14:15], v[14:15], v[146:147]
	v_med3_f32 v16, v16, s65, v179
	v_pk_add_f32 v[146:147], v[148:149], 1.0 op_sel_hi:[1,0]
	v_mov_b32_e32 v149, v167
	v_cvt_pk_fp8_f32 v149, v14, v15
	v_pk_fma_f32 v[14:15], v[138:139], s[30:31], v[30:31] op_sel_hi:[1,0,1]
	v_med3_f32 v17, v17, s65, v179
	v_mov_b32_e32 v148, v167
	v_min_f32_e32 v14, 0x40e00000, v14
	v_min_f32_e32 v15, 0x40e00000, v15
	v_cvt_pk_fp8_f32 v148, v10, v11
	v_pk_fma_f32 v[10:11], v[16:17], v[12:13], v[12:13]
	v_pk_mul_f32 v[16:17], v[14:15], s[34:35] op_sel_hi:[1,0]
	v_pk_fma_f32 v[12:13], v[140:141], s[30:31], v[32:33] op_sel_hi:[1,0,1]
	v_exp_f32_e32 v16, v16
	v_exp_f32_e32 v17, v17
	v_min_f32_e32 v12, 0x40e00000, v12
	v_min_f32_e32 v13, 0x40e00000, v13
	v_pk_fma_f32 v[140:141], v[142:143], s[30:31], v[26:27] op_sel_hi:[1,0,1]
	v_pk_add_f32 v[16:17], v[16:17], 1.0 op_sel_hi:[1,0]
	v_pk_mul_f32 v[142:143], v[12:13], s[34:35] op_sel_hi:[1,0]
	v_rcp_f32_e32 v16, v16
	v_rcp_f32_e32 v17, v17
	v_exp_f32_e32 v142, v142
	v_exp_f32_e32 v143, v143
	v_med3_f32 v140, v140, s65, v179
	v_med3_f32 v141, v141, s65, v179
	v_pk_fma_f32 v[14:15], v[140:141], v[14:15], v[14:15]
	v_pk_fma_f32 v[138:139], v[144:145], s[30:31], v[28:29] op_sel_hi:[1,0,1]
	v_pk_mul_f32 v[14:15], v[14:15], v[16:17]
	v_pk_add_f32 v[16:17], v[142:143], 1.0 op_sel_hi:[1,0]
	v_med3_f32 v138, v138, s65, v179
	v_rcp_f32_e32 v16, v16
	v_rcp_f32_e32 v17, v17
	v_med3_f32 v139, v139, s65, v179
	v_pk_fma_f32 v[130:131], v[130:131], s[30:31], v[22:23] op_sel_hi:[1,0,1]
	v_pk_fma_f32 v[12:13], v[138:139], v[12:13], v[12:13]
	v_min_f32_e32 v130, 0x40e00000, v130
	v_min_f32_e32 v131, 0x40e00000, v131
	v_pk_mul_f32 v[12:13], v[12:13], v[16:17]
	v_pk_fma_f32 v[16:17], v[132:133], s[30:31], v[24:25] op_sel_hi:[1,0,1]
	v_pk_fma_f32 v[132:133], v[136:137], s[30:31], v[20:21] op_sel_hi:[1,0,1]
	v_pk_mul_f32 v[136:137], v[130:131], s[34:35] op_sel_hi:[1,0]
	v_pk_fma_f32 v[134:135], v[134:135], s[30:31], v[18:19] op_sel_hi:[1,0,1]
	v_exp_f32_e32 v136, v136
	v_exp_f32_e32 v137, v137
	v_med3_f32 v134, v134, s65, v179
	v_med3_f32 v135, v135, s65, v179
	v_min_f32_e32 v16, 0x40e00000, v16
	v_min_f32_e32 v17, 0x40e00000, v17
	v_readfirstlane_b32 s99, v0
	s_cmpk_gt_u32 s99, 0xff
	s_cbranch_scc1 .Lz0_1442
	s_barrier
.Lz0_1442:
	v_pk_fma_f32 v[130:131], v[134:135], v[130:131], v[130:131]
	v_pk_mul_f32 v[134:135], v[16:17], s[34:35] op_sel_hi:[1,0]
	v_pk_add_f32 v[136:137], v[136:137], 1.0 op_sel_hi:[1,0]
	v_exp_f32_e32 v134, v134
	v_exp_f32_e32 v135, v135
	v_rcp_f32_e32 v136, v136
	v_rcp_f32_e32 v137, v137
	v_med3_f32 v132, v132, s65, v179
	v_pk_add_f32 v[134:135], v[134:135], 1.0 op_sel_hi:[1,0]
	v_med3_f32 v133, v133, s65, v179
	v_pk_mul_f32 v[130:131], v[130:131], v[136:137]
	v_rcp_f32_e32 v134, v134
	v_rcp_f32_e32 v135, v135
	v_mov_b32_e32 v137, v167
	v_cvt_pk_fp8_f32 v137, v130, v131
	v_mov_b32_e32 v136, v167
	v_cvt_pk_fp8_f32 v136, v14, v15
	v_pk_fma_f32 v[14:15], v[132:133], v[16:17], v[16:17]
	v_pk_fma_f32 v[114:115], v[114:115], s[30:31], v[22:23] op_sel_hi:[1,0,1]
	v_pk_mul_f32 v[14:15], v[14:15], v[134:135]
	v_cvt_pk_fp8_f32 v136, v12, v13 op_sel:[0,0,1]
	v_cvt_pk_fp8_f32 v137, v14, v15 op_sel:[0,0,1]
	v_pk_fma_f32 v[14:15], v[122:123], s[30:31], v[30:31] op_sel_hi:[1,0,1]
	v_pk_fma_f32 v[12:13], v[124:125], s[30:31], v[32:33] op_sel_hi:[1,0,1]
	v_min_f32_e32 v14, 0x40e00000, v14
	v_min_f32_e32 v15, 0x40e00000, v15
	v_pk_mul_f32 v[16:17], v[14:15], s[34:35] op_sel_hi:[1,0]
	v_min_f32_e32 v12, 0x40e00000, v12
	v_exp_f32_e32 v16, v16
	v_exp_f32_e32 v17, v17
	v_min_f32_e32 v13, 0x40e00000, v13
	v_pk_fma_f32 v[124:125], v[126:127], s[30:31], v[26:27] op_sel_hi:[1,0,1]
	v_pk_mul_f32 v[126:127], v[12:13], s[34:35] op_sel_hi:[1,0]
	v_pk_add_f32 v[16:17], v[16:17], 1.0 op_sel_hi:[1,0]
	v_exp_f32_e32 v126, v126
	v_rcp_f32_e32 v16, v16
	v_rcp_f32_e32 v17, v17
	v_exp_f32_e32 v127, v127
	v_med3_f32 v124, v124, s65, v179
	v_med3_f32 v125, v125, s65, v179
	v_pk_fma_f32 v[14:15], v[124:125], v[14:15], v[14:15]
	v_pk_fma_f32 v[122:123], v[128:129], s[30:31], v[28:29] op_sel_hi:[1,0,1]
	v_pk_mul_f32 v[14:15], v[14:15], v[16:17]
	v_pk_add_f32 v[16:17], v[126:127], 1.0 op_sel_hi:[1,0]
	v_med3_f32 v122, v122, s65, v179
	v_rcp_f32_e32 v16, v16
	v_rcp_f32_e32 v17, v17
	v_med3_f32 v123, v123, s65, v179
	v_pk_fma_f32 v[12:13], v[122:123], v[12:13], v[12:13]
	v_min_f32_e32 v114, 0x40e00000, v114
	v_min_f32_e32 v115, 0x40e00000, v115
	v_pk_mul_f32 v[12:13], v[12:13], v[16:17]
	v_pk_fma_f32 v[16:17], v[116:117], s[30:31], v[24:25] op_sel_hi:[1,0,1]
	v_pk_fma_f32 v[116:117], v[120:121], s[30:31], v[20:21] op_sel_hi:[1,0,1]
	v_pk_mul_f32 v[120:121], v[114:115], s[34:35] op_sel_hi:[1,0]
	v_pk_fma_f32 v[118:119], v[118:119], s[30:31], v[18:19] op_sel_hi:[1,0,1]
	v_exp_f32_e32 v120, v120
	v_exp_f32_e32 v121, v121
	v_med3_f32 v118, v118, s65, v179
	v_med3_f32 v119, v119, s65, v179
	v_min_f32_e32 v16, 0x40e00000, v16
	v_min_f32_e32 v17, 0x40e00000, v17
	v_rcp_f32_e32 v146, v146
	v_rcp_f32_e32 v147, v147
	v_pk_add_f32 v[120:121], v[120:121], 1.0 op_sel_hi:[1,0]
	v_pk_fma_f32 v[114:115], v[118:119], v[114:115], v[114:115]
	v_pk_mul_f32 v[118:119], v[16:17], s[34:35] op_sel_hi:[1,0]
	v_rcp_f32_e32 v120, v120
	v_rcp_f32_e32 v121, v121
	v_exp_f32_e32 v118, v118
	v_exp_f32_e32 v119, v119
	s_lshr_b32 s39, s39, 1
	v_pk_mul_f32 v[10:11], v[10:11], v[146:147]
	s_lshl_b32 s41, s44, 7
	s_and_b32 s39, s39, 0x60
	v_cvt_pk_fp8_f32 v149, v10, v11 op_sel:[0,0,1]
	v_or_b32_e32 v10, 16, v6
	v_pk_mul_f32 v[114:115], v[114:115], v[120:121]
	v_pk_add_f32 v[118:119], v[118:119], 1.0 op_sel_hi:[1,0]
	v_mov_b32_e32 v120, v167
	s_or_b32 s41, s39, s41
	v_ashrrev_i32_e32 v11, 31, v10
	v_rcp_f32_e32 v118, v118
	v_rcp_f32_e32 v119, v119
	v_cvt_pk_fp8_f32 v120, v14, v15
	v_mov_b32_e32 v121, v167
	v_or_b32_e32 v4, s41, v8
	v_lshlrev_b64 v[10:11], 11, v[10:11]
	v_cvt_pk_fp8_f32 v121, v114, v115
	v_ashrrev_i32_e32 v5, 31, v4
	v_lshl_add_u64 v[10:11], s[16:17], 0, v[10:11]
	v_med3_f32 v116, v116, s65, v179
	v_med3_f32 v117, v117, s65, v179
	v_lshl_add_u64 v[10:11], v[10:11], 0, v[4:5]
	v_pk_fma_f32 v[14:15], v[116:117], v[16:17], v[16:17]
	global_store_dwordx2 v[10:11], v[136:137], off
	v_or_b32_e32 v10, 32, v6
	v_pk_mul_f32 v[14:15], v[14:15], v[118:119]
	v_cvt_pk_fp8_f32 v120, v12, v13 op_sel:[0,0,1]
	v_pk_fma_f32 v[12:13], v[106:107], s[30:31], v[30:31] op_sel_hi:[1,0,1]
	v_ashrrev_i32_e32 v11, 31, v10
	v_cvt_pk_fp8_f32 v121, v14, v15 op_sel:[0,0,1]
	v_min_f32_e32 v12, 0x40e00000, v12
	v_min_f32_e32 v13, 0x40e00000, v13
	v_lshlrev_b64 v[10:11], 11, v[10:11]
	v_pk_mul_f32 v[14:15], v[12:13], s[34:35] op_sel_hi:[1,0]
	v_lshl_add_u64 v[10:11], s[16:17], 0, v[10:11]
	v_exp_f32_e32 v14, v14
	v_exp_f32_e32 v15, v15
	v_lshl_add_u64 v[10:11], v[10:11], 0, v[4:5]
	global_store_dwordx2 v[10:11], v[120:121], off
	v_pk_fma_f32 v[10:11], v[108:109], s[30:31], v[32:33] op_sel_hi:[1,0,1]
	v_pk_add_f32 v[14:15], v[14:15], 1.0 op_sel_hi:[1,0]
	v_min_f32_e32 v10, 0x40e00000, v10
	v_min_f32_e32 v11, 0x40e00000, v11
	v_pk_mul_f32 v[108:109], v[10:11], s[34:35] op_sel_hi:[1,0]
	v_rcp_f32_e32 v14, v14
	v_rcp_f32_e32 v15, v15
	v_exp_f32_e32 v108, v108
	v_exp_f32_e32 v109, v109
	v_pk_fma_f32 v[106:107], v[110:111], s[30:31], v[26:27] op_sel_hi:[1,0,1]
	v_pk_fma_f32 v[16:17], v[112:113], s[30:31], v[28:29] op_sel_hi:[1,0,1]
	v_med3_f32 v106, v106, s65, v179
	v_med3_f32 v107, v107, s65, v179
	v_pk_fma_f32 v[12:13], v[106:107], v[12:13], v[12:13]
	v_med3_f32 v16, v16, s65, v179
	v_pk_mul_f32 v[12:13], v[12:13], v[14:15]
	v_pk_add_f32 v[14:15], v[108:109], 1.0 op_sel_hi:[1,0]
	v_med3_f32 v17, v17, s65, v179
	v_rcp_f32_e32 v14, v14
	v_rcp_f32_e32 v15, v15
	v_pk_fma_f32 v[10:11], v[16:17], v[10:11], v[10:11]
	v_pk_fma_f32 v[16:17], v[90:91], s[30:31], v[22:23] op_sel_hi:[1,0,1]
	v_pk_fma_f32 v[98:99], v[98:99], s[30:31], v[18:19] op_sel_hi:[1,0,1]
	v_min_f32_e32 v16, 0x40e00000, v16
	v_min_f32_e32 v17, 0x40e00000, v17
	v_pk_mul_f32 v[10:11], v[10:11], v[14:15]
	v_pk_fma_f32 v[14:15], v[92:93], s[30:31], v[24:25] op_sel_hi:[1,0,1]
	v_pk_mul_f32 v[92:93], v[16:17], s[34:35] op_sel_hi:[1,0]
	v_med3_f32 v98, v98, s65, v179
	v_exp_f32_e32 v92, v92
	v_exp_f32_e32 v93, v93
	v_med3_f32 v99, v99, s65, v179
	v_min_f32_e32 v14, 0x40e00000, v14
	v_min_f32_e32 v15, 0x40e00000, v15
	v_pk_add_f32 v[92:93], v[92:93], 1.0 op_sel_hi:[1,0]
	v_pk_fma_f32 v[16:17], v[98:99], v[16:17], v[16:17]
	v_pk_mul_f32 v[98:99], v[14:15], s[34:35] op_sel_hi:[1,0]
	v_rcp_f32_e32 v92, v92
	v_rcp_f32_e32 v93, v93
	v_exp_f32_e32 v98, v98
	v_exp_f32_e32 v99, v99
	v_ashrrev_i32_e32 v7, 31, v6
	v_pk_mul_f32 v[16:17], v[16:17], v[92:93]
	v_cvt_pk_fp8_f32 v148, v2, v3 op_sel:[0,0,1]
	v_pk_add_f32 v[92:93], v[98:99], 1.0 op_sel_hi:[1,0]
	v_lshlrev_b64 v[2:3], 11, v[6:7]
	v_or_b32_e32 v6, 48, v6
	v_rcp_f32_e32 v92, v92
	v_rcp_f32_e32 v93, v93
	v_mov_b32_e32 v98, v167
	v_mov_b32_e32 v99, v167
	v_ashrrev_i32_e32 v7, 31, v6
	v_pk_fma_f32 v[90:91], v[100:101], s[30:31], v[20:21] op_sel_hi:[1,0,1]
	v_cvt_pk_fp8_f32 v98, v12, v13
	v_cvt_pk_fp8_f32 v99, v16, v17
	v_med3_f32 v90, v90, s65, v179
	v_med3_f32 v91, v91, s65, v179
	v_lshlrev_b64 v[6:7], 11, v[6:7]
	v_lshl_add_u64 v[2:3], s[16:17], 0, v[2:3]
	v_pk_fma_f32 v[12:13], v[90:91], v[14:15], v[14:15]
	v_lshl_add_u64 v[6:7], s[16:17], 0, v[6:7]
	v_lshl_add_u64 v[2:3], v[2:3], 0, v[4:5]
	v_pk_mul_f32 v[12:13], v[12:13], v[92:93]
	v_lshl_add_u64 v[4:5], v[6:7], 0, v[4:5]
	v_pk_fma_f32 v[6:7], v[94:95], s[30:31], v[30:31] op_sel_hi:[1,0,1]
	v_cvt_pk_fp8_f32 v98, v10, v11 op_sel:[0,0,1]
	v_cvt_pk_fp8_f32 v99, v12, v13 op_sel:[0,0,1]
	v_min_f32_e32 v6, 0x40e00000, v6
	v_min_f32_e32 v7, 0x40e00000, v7
	v_pk_mul_f32 v[10:11], v[6:7], s[34:35] op_sel_hi:[1,0]
	global_store_dwordx2 v[4:5], v[98:99], off
	v_exp_f32_e32 v10, v10
	v_exp_f32_e32 v11, v11
	v_pk_fma_f32 v[4:5], v[96:97], s[30:31], v[32:33] op_sel_hi:[1,0,1]
	v_pk_fma_f32 v[14:15], v[102:103], s[30:31], v[26:27] op_sel_hi:[1,0,1]
	v_min_f32_e32 v4, 0x40e00000, v4
	v_min_f32_e32 v5, 0x40e00000, v5
	v_pk_add_f32 v[10:11], v[10:11], 1.0 op_sel_hi:[1,0]
	v_pk_mul_f32 v[16:17], v[4:5], s[34:35] op_sel_hi:[1,0]
	v_rcp_f32_e32 v10, v10
	v_rcp_f32_e32 v11, v11
	v_exp_f32_e32 v16, v16
	v_exp_f32_e32 v17, v17
	v_pk_fma_f32 v[12:13], v[104:105], s[30:31], v[28:29] op_sel_hi:[1,0,1]
	v_med3_f32 v14, v14, s65, v179
	v_med3_f32 v15, v15, s65, v179
	v_pk_fma_f32 v[6:7], v[14:15], v[6:7], v[6:7]
	v_med3_f32 v12, v12, s65, v179
	v_med3_f32 v13, v13, s65, v179
	v_pk_mul_f32 v[6:7], v[6:7], v[10:11]
	v_pk_add_f32 v[10:11], v[16:17], 1.0 op_sel_hi:[1,0]
	v_pk_fma_f32 v[4:5], v[12:13], v[4:5], v[4:5]
	v_pk_fma_f32 v[12:13], v[82:83], s[30:31], v[22:23] op_sel_hi:[1,0,1]
	v_rcp_f32_e32 v10, v10
	v_rcp_f32_e32 v11, v11
	v_min_f32_e32 v12, 0x40e00000, v12
	v_min_f32_e32 v13, 0x40e00000, v13
	v_pk_mul_f32 v[16:17], v[12:13], s[34:35] op_sel_hi:[1,0]
	v_pk_mul_f32 v[4:5], v[4:5], v[10:11]
	v_exp_f32_e32 v16, v16
	v_exp_f32_e32 v17, v17
	v_pk_fma_f32 v[10:11], v[84:85], s[30:31], v[24:25] op_sel_hi:[1,0,1]
	v_pk_fma_f32 v[82:83], v[86:87], s[30:31], v[18:19] op_sel_hi:[1,0,1]
	v_min_f32_e32 v10, 0x40e00000, v10
	v_med3_f32 v82, v82, s65, v179
	v_med3_f32 v83, v83, s65, v179
	v_min_f32_e32 v11, 0x40e00000, v11
	v_pk_add_f32 v[16:17], v[16:17], 1.0 op_sel_hi:[1,0]
	v_pk_fma_f32 v[12:13], v[82:83], v[12:13], v[12:13]
	v_pk_mul_f32 v[82:83], v[10:11], s[34:35] op_sel_hi:[1,0]
	v_rcp_f32_e32 v16, v16
	v_rcp_f32_e32 v17, v17
	v_exp_f32_e32 v82, v82
	v_exp_f32_e32 v83, v83
	v_pk_fma_f32 v[14:15], v[88:89], s[30:31], v[20:21] op_sel_hi:[1,0,1]
	v_pk_mul_f32 v[12:13], v[12:13], v[16:17]
	v_med3_f32 v14, v14, s65, v179
	v_pk_add_f32 v[16:17], v[82:83], 1.0 op_sel_hi:[1,0]
	v_mov_b32_e32 v83, v167
	v_rcp_f32_e32 v16, v16
	v_rcp_f32_e32 v17, v17
	v_mov_b32_e32 v82, v167
	v_cvt_pk_fp8_f32 v83, v12, v13
	v_med3_f32 v15, v15, s65, v179
	v_cvt_pk_fp8_f32 v82, v6, v7
	v_pk_fma_f32 v[6:7], v[14:15], v[10:11], v[10:11]
	s_mov_b32 s41, 0x40000
	v_pk_mul_f32 v[6:7], v[6:7], v[16:17]
	v_cvt_pk_fp8_f32 v82, v4, v5 op_sel:[0,0,1]
	v_cvt_pk_fp8_f32 v83, v6, v7 op_sel:[0,0,1]
	v_pk_fma_f32 v[6:7], v[74:75], s[30:31], v[30:31] op_sel_hi:[1,0,1]
	v_add_co_u32_e32 v4, vcc, s41, v2
	v_min_f32_e32 v6, 0x40e00000, v6
	v_min_f32_e32 v7, 0x40e00000, v7
	v_pk_mul_f32 v[10:11], v[6:7], s[34:35] op_sel_hi:[1,0]
	v_addc_co_u32_e32 v5, vcc, 0, v3, vcc
	v_exp_f32_e32 v10, v10
	v_exp_f32_e32 v11, v11
	global_store_dwordx2 v[4:5], v[82:83], off
	v_pk_fma_f32 v[4:5], v[76:77], s[30:31], v[32:33] op_sel_hi:[1,0,1]
	v_pk_fma_f32 v[14:15], v[78:79], s[30:31], v[26:27] op_sel_hi:[1,0,1]
	v_min_f32_e32 v4, 0x40e00000, v4
	v_min_f32_e32 v5, 0x40e00000, v5
	v_pk_add_f32 v[10:11], v[10:11], 1.0 op_sel_hi:[1,0]
	v_pk_mul_f32 v[16:17], v[4:5], s[34:35] op_sel_hi:[1,0]
	v_rcp_f32_e32 v10, v10
	v_rcp_f32_e32 v11, v11
	v_exp_f32_e32 v16, v16
	v_exp_f32_e32 v17, v17
	v_pk_fma_f32 v[12:13], v[80:81], s[30:31], v[28:29] op_sel_hi:[1,0,1]
	v_med3_f32 v14, v14, s65, v179
	v_med3_f32 v15, v15, s65, v179
	v_pk_fma_f32 v[6:7], v[14:15], v[6:7], v[6:7]
	v_med3_f32 v12, v12, s65, v179
	v_med3_f32 v13, v13, s65, v179
	v_pk_mul_f32 v[6:7], v[6:7], v[10:11]
	v_pk_add_f32 v[10:11], v[16:17], 1.0 op_sel_hi:[1,0]
	v_pk_fma_f32 v[4:5], v[12:13], v[4:5], v[4:5]
	v_pk_fma_f32 v[12:13], v[66:67], s[30:31], v[22:23] op_sel_hi:[1,0,1]
	v_rcp_f32_e32 v10, v10
	v_rcp_f32_e32 v11, v11
	v_min_f32_e32 v12, 0x40e00000, v12
	v_min_f32_e32 v13, 0x40e00000, v13
	v_pk_mul_f32 v[16:17], v[12:13], s[34:35] op_sel_hi:[1,0]
	v_pk_mul_f32 v[4:5], v[4:5], v[10:11]
	v_exp_f32_e32 v16, v16
	v_exp_f32_e32 v17, v17
	v_pk_fma_f32 v[10:11], v[68:69], s[30:31], v[24:25] op_sel_hi:[1,0,1]
	v_pk_fma_f32 v[66:67], v[70:71], s[30:31], v[18:19] op_sel_hi:[1,0,1]
	v_min_f32_e32 v10, 0x40e00000, v10
	v_med3_f32 v66, v66, s65, v179
	v_med3_f32 v67, v67, s65, v179
	v_min_f32_e32 v11, 0x40e00000, v11
	v_pk_add_f32 v[16:17], v[16:17], 1.0 op_sel_hi:[1,0]
	v_pk_fma_f32 v[12:13], v[66:67], v[12:13], v[12:13]
	v_pk_mul_f32 v[66:67], v[10:11], s[34:35] op_sel_hi:[1,0]
	v_rcp_f32_e32 v16, v16
	v_rcp_f32_e32 v17, v17
	v_exp_f32_e32 v66, v66
	v_exp_f32_e32 v67, v67
	v_pk_fma_f32 v[14:15], v[72:73], s[30:31], v[20:21] op_sel_hi:[1,0,1]
	v_pk_mul_f32 v[12:13], v[12:13], v[16:17]
	v_med3_f32 v14, v14, s65, v179
	v_pk_add_f32 v[16:17], v[66:67], 1.0 op_sel_hi:[1,0]
	v_mov_b32_e32 v67, v167
	v_rcp_f32_e32 v16, v16
	v_rcp_f32_e32 v17, v17
	v_mov_b32_e32 v66, v167
	v_cvt_pk_fp8_f32 v67, v12, v13
	v_med3_f32 v15, v15, s65, v179
	v_cvt_pk_fp8_f32 v66, v6, v7
	v_pk_fma_f32 v[6:7], v[14:15], v[10:11], v[10:11]
	s_mov_b32 s41, 0x48000
	v_pk_mul_f32 v[6:7], v[6:7], v[16:17]
	v_cvt_pk_fp8_f32 v66, v4, v5 op_sel:[0,0,1]
	v_cvt_pk_fp8_f32 v67, v6, v7 op_sel:[0,0,1]
	v_pk_fma_f32 v[6:7], v[58:59], s[30:31], v[30:31] op_sel_hi:[1,0,1]
	v_add_co_u32_e32 v4, vcc, s41, v2
	v_min_f32_e32 v6, 0x40e00000, v6
	v_min_f32_e32 v7, 0x40e00000, v7
	v_pk_mul_f32 v[10:11], v[6:7], s[34:35] op_sel_hi:[1,0]
	v_addc_co_u32_e32 v5, vcc, 0, v3, vcc
	v_exp_f32_e32 v10, v10
	v_exp_f32_e32 v11, v11
	global_store_dwordx2 v[4:5], v[66:67], off
	v_pk_fma_f32 v[4:5], v[60:61], s[30:31], v[32:33] op_sel_hi:[1,0,1]
	v_pk_fma_f32 v[14:15], v[62:63], s[30:31], v[26:27] op_sel_hi:[1,0,1]
	v_min_f32_e32 v4, 0x40e00000, v4
	v_min_f32_e32 v5, 0x40e00000, v5
	v_pk_add_f32 v[10:11], v[10:11], 1.0 op_sel_hi:[1,0]
	v_pk_mul_f32 v[16:17], v[4:5], s[34:35] op_sel_hi:[1,0]
	v_rcp_f32_e32 v10, v10
	v_rcp_f32_e32 v11, v11
	v_exp_f32_e32 v16, v16
	v_exp_f32_e32 v17, v17
	v_pk_fma_f32 v[12:13], v[64:65], s[30:31], v[28:29] op_sel_hi:[1,0,1]
	v_med3_f32 v14, v14, s65, v179
	v_med3_f32 v15, v15, s65, v179
	v_pk_fma_f32 v[6:7], v[14:15], v[6:7], v[6:7]
	v_med3_f32 v12, v12, s65, v179
	v_med3_f32 v13, v13, s65, v179
	v_pk_mul_f32 v[6:7], v[6:7], v[10:11]
	v_pk_add_f32 v[10:11], v[16:17], 1.0 op_sel_hi:[1,0]
	v_pk_fma_f32 v[4:5], v[12:13], v[4:5], v[4:5]
	v_pk_fma_f32 v[12:13], v[50:51], s[30:31], v[22:23] op_sel_hi:[1,0,1]
	v_rcp_f32_e32 v10, v10
	v_rcp_f32_e32 v11, v11
	v_min_f32_e32 v12, 0x40e00000, v12
	v_min_f32_e32 v13, 0x40e00000, v13
	v_pk_mul_f32 v[16:17], v[12:13], s[34:35] op_sel_hi:[1,0]
	v_pk_mul_f32 v[4:5], v[4:5], v[10:11]
	v_exp_f32_e32 v16, v16
	v_exp_f32_e32 v17, v17
	v_pk_fma_f32 v[10:11], v[52:53], s[30:31], v[24:25] op_sel_hi:[1,0,1]
	v_pk_fma_f32 v[50:51], v[54:55], s[30:31], v[18:19] op_sel_hi:[1,0,1]
	v_min_f32_e32 v10, 0x40e00000, v10
	v_med3_f32 v50, v50, s65, v179
	v_med3_f32 v51, v51, s65, v179
	v_min_f32_e32 v11, 0x40e00000, v11
	v_pk_add_f32 v[16:17], v[16:17], 1.0 op_sel_hi:[1,0]
	v_pk_fma_f32 v[12:13], v[50:51], v[12:13], v[12:13]
	v_pk_mul_f32 v[50:51], v[10:11], s[34:35] op_sel_hi:[1,0]
	v_rcp_f32_e32 v16, v16
	v_rcp_f32_e32 v17, v17
	v_exp_f32_e32 v50, v50
	v_exp_f32_e32 v51, v51
	v_pk_fma_f32 v[14:15], v[56:57], s[30:31], v[20:21] op_sel_hi:[1,0,1]
	v_pk_mul_f32 v[12:13], v[12:13], v[16:17]
	v_med3_f32 v14, v14, s65, v179
	v_pk_add_f32 v[16:17], v[50:51], 1.0 op_sel_hi:[1,0]
	v_mov_b32_e32 v51, v167
	v_rcp_f32_e32 v16, v16
	v_rcp_f32_e32 v17, v17
	v_mov_b32_e32 v50, v167
	v_cvt_pk_fp8_f32 v51, v12, v13
	v_med3_f32 v15, v15, s65, v179
	v_cvt_pk_fp8_f32 v50, v6, v7
	v_pk_fma_f32 v[6:7], v[14:15], v[10:11], v[10:11]
	s_mov_b32 s41, 0x50000
	v_pk_mul_f32 v[6:7], v[6:7], v[16:17]
	v_cvt_pk_fp8_f32 v50, v4, v5 op_sel:[0,0,1]
	v_cvt_pk_fp8_f32 v51, v6, v7 op_sel:[0,0,1]
	v_pk_fma_f32 v[6:7], v[42:43], s[30:31], v[30:31] op_sel_hi:[1,0,1]
	v_add_co_u32_e32 v4, vcc, s41, v2
	v_min_f32_e32 v6, 0x40e00000, v6
	v_min_f32_e32 v7, 0x40e00000, v7
	v_pk_mul_f32 v[10:11], v[6:7], s[34:35] op_sel_hi:[1,0]
	v_addc_co_u32_e32 v5, vcc, 0, v3, vcc
	v_exp_f32_e32 v10, v10
	v_exp_f32_e32 v11, v11
	global_store_dwordx2 v[4:5], v[50:51], off
	v_pk_fma_f32 v[4:5], v[44:45], s[30:31], v[32:33] op_sel_hi:[1,0,1]
	v_pk_fma_f32 v[14:15], v[46:47], s[30:31], v[26:27] op_sel_hi:[1,0,1]
	v_min_f32_e32 v4, 0x40e00000, v4
	v_min_f32_e32 v5, 0x40e00000, v5
	v_pk_add_f32 v[10:11], v[10:11], 1.0 op_sel_hi:[1,0]
	v_pk_mul_f32 v[16:17], v[4:5], s[34:35] op_sel_hi:[1,0]
	v_rcp_f32_e32 v10, v10
	v_rcp_f32_e32 v11, v11
	v_exp_f32_e32 v16, v16
	v_exp_f32_e32 v17, v17
	v_pk_fma_f32 v[12:13], v[48:49], s[30:31], v[28:29] op_sel_hi:[1,0,1]
	v_med3_f32 v14, v14, s65, v179
	v_med3_f32 v15, v15, s65, v179
	v_pk_fma_f32 v[6:7], v[14:15], v[6:7], v[6:7]
	v_med3_f32 v12, v12, s65, v179
	v_med3_f32 v13, v13, s65, v179
	v_pk_mul_f32 v[6:7], v[6:7], v[10:11]
	v_pk_add_f32 v[10:11], v[16:17], 1.0 op_sel_hi:[1,0]
	v_pk_fma_f32 v[4:5], v[12:13], v[4:5], v[4:5]
	v_pk_fma_f32 v[12:13], v[34:35], s[30:31], v[22:23] op_sel_hi:[1,0,1]
	v_rcp_f32_e32 v10, v10
	v_rcp_f32_e32 v11, v11
	v_min_f32_e32 v12, 0x40e00000, v12
	v_min_f32_e32 v13, 0x40e00000, v13
	v_pk_mul_f32 v[16:17], v[12:13], s[34:35] op_sel_hi:[1,0]
	v_pk_mul_f32 v[4:5], v[4:5], v[10:11]
	v_exp_f32_e32 v16, v16
	v_exp_f32_e32 v17, v17
	v_pk_fma_f32 v[10:11], v[36:37], s[30:31], v[24:25] op_sel_hi:[1,0,1]
	v_pk_fma_f32 v[18:19], v[38:39], s[30:31], v[18:19] op_sel_hi:[1,0,1]
	v_min_f32_e32 v10, 0x40e00000, v10
	v_med3_f32 v18, v18, s65, v179
	v_med3_f32 v19, v19, s65, v179
	v_min_f32_e32 v11, 0x40e00000, v11
	v_pk_add_f32 v[16:17], v[16:17], 1.0 op_sel_hi:[1,0]
	v_pk_fma_f32 v[12:13], v[18:19], v[12:13], v[12:13]
	v_pk_mul_f32 v[18:19], v[10:11], s[34:35] op_sel_hi:[1,0]
	v_rcp_f32_e32 v16, v16
	v_rcp_f32_e32 v17, v17
	v_exp_f32_e32 v18, v18
	v_exp_f32_e32 v19, v19
	v_pk_fma_f32 v[14:15], v[40:41], s[30:31], v[20:21] op_sel_hi:[1,0,1]
	v_pk_mul_f32 v[12:13], v[12:13], v[16:17]
	v_med3_f32 v14, v14, s65, v179
	v_pk_add_f32 v[16:17], v[18:19], 1.0 op_sel_hi:[1,0]
	v_mov_b32_e32 v18, v167
	v_rcp_f32_e32 v16, v16
	v_rcp_f32_e32 v17, v17
	v_mov_b32_e32 v19, v167
	v_cvt_pk_fp8_f32 v18, v6, v7
	v_cvt_pk_fp8_f32 v19, v12, v13
	v_med3_f32 v15, v15, s65, v179
	v_pk_fma_f32 v[6:7], v[14:15], v[10:11], v[10:11]
	v_cvt_pk_fp8_f32 v18, v4, v5 op_sel:[0,0,1]
	v_pk_mul_f32 v[6:7], v[6:7], v[16:17]
	global_store_dwordx2 v[2:3], v[148:149], off
	v_cvt_pk_fp8_f32 v19, v6, v7 op_sel:[0,0,1]
	v_add_co_u32_e32 v2, vcc, 0x58000, v2
	s_mov_b64 s[44:45], -1
	s_nop 0
	v_addc_co_u32_e32 v3, vcc, 0, v3, vcc
	s_and_b64 vcc, s[42:43], exec
	global_store_dwordx2 v[2:3], v[18:19], off
	v_readfirstlane_b32 s99, v0
	s_cmpk_gt_u32 s99, 0xff
	s_cbranch_scc0 .Lz1_1442
	s_barrier

.LBB0_1547:
	ds_read_b128 v[10:13], v183
	ds_read_b128 v[14:17], v183 offset:1024
	ds_read_b128 v[174:177], v183 offset:2048
	ds_read_b128 v[178:181], v183 offset:3072
	s_add_u32 s46, s44, 0xfffc0080
	s_addc_u32 s47, s45, -1
	s_cmp_eq_u32 s80, 12
	s_cselect_b32 s49, s27, s47
	s_cselect_b32 s48, s31, s46
	s_cselect_b32 s47, s25, s79
	s_cselect_b32 s46, s39, s78
	s_mov_b32 m0, s68
	v_lshl_add_u64 v[2:3], s[44:45], 0, v[170:171]
	ds_read_b128 v[188:191], v184
	ds_read_b128 v[192:195], v184 offset:1024
	ds_read_b128 v[196:199], v184 offset:2048
	ds_read_b128 v[200:203], v184 offset:3072
	ds_read_b128 v[204:207], v184 offset:4096
	ds_read_b128 v[208:211], v184 offset:5120
	ds_read_b128 v[212:215], v184 offset:6144
	ds_read_b128 v[216:219], v184 offset:7168
	global_load_lds_dwordx4 v[2:3], off
	v_lshl_add_u64 v[2:3], s[44:45], 0, v[172:173]
	s_mov_b32 m0, s69
	s_nop 0
	global_load_lds_dwordx4 v[2:3], off
	ds_read_b128 v[220:223], v185
	ds_read_b128 v[224:227], v185 offset:1024
	ds_read_b128 v[228:231], v185 offset:2048
	ds_read_b128 v[232:235], v185 offset:3072
	s_waitcnt vmcnt(8) lgkmcnt(0)
	s_barrier
	s_setprio 1
	v_mfma_f32_16x16x128_f8f6f4 v[150:153], v[10:17], v[188:195], v[150:153]
	v_mfma_f32_16x16x128_f8f6f4 v[146:149], v[174:181], v[188:195], v[146:149]
	v_mfma_f32_16x16x128_f8f6f4 v[134:137], v[10:17], v[196:203], v[134:137]
	v_mfma_f32_16x16x128_f8f6f4 v[130:133], v[174:181], v[196:203], v[130:133]
	v_mfma_f32_16x16x128_f8f6f4 v[118:121], v[10:17], v[204:211], v[118:121]
	v_mfma_f32_16x16x128_f8f6f4 v[114:117], v[174:181], v[204:211], v[114:117]
	v_mfma_f32_16x16x128_f8f6f4 v[86:89], v[10:17], v[212:219], v[86:89]
	v_mfma_f32_16x16x128_f8f6f4 v[82:85], v[174:181], v[212:219], v[82:85]
	v_mfma_f32_16x16x128_f8f6f4 v[158:161], v[220:227], v[188:195], v[158:161]
	v_mfma_f32_16x16x128_f8f6f4 v[154:157], v[228:235], v[188:195], v[154:157]
	v_mfma_f32_16x16x128_f8f6f4 v[142:145], v[220:227], v[196:203], v[142:145]
	v_mfma_f32_16x16x128_f8f6f4 v[138:141], v[228:235], v[196:203], v[138:141]
	v_mfma_f32_16x16x128_f8f6f4 v[126:129], v[220:227], v[204:211], v[126:129]
	v_mfma_f32_16x16x128_f8f6f4 v[122:125], v[228:235], v[204:211], v[122:125]
	v_mfma_f32_16x16x128_f8f6f4 v[94:97], v[220:227], v[212:219], v[94:97]
	v_mfma_f32_16x16x128_f8f6f4 v[90:93], v[228:235], v[212:219], v[90:93]
	s_setprio 0
	s_barrier
	ds_read_b128 v[188:191], v184 offset:16384
	ds_read_b128 v[192:195], v184 offset:17408
	ds_read_b128 v[196:199], v184 offset:18432
	ds_read_b128 v[200:203], v184 offset:19456
	ds_read_b128 v[204:207], v184 offset:20480
	ds_read_b128 v[208:211], v184 offset:21504
	ds_read_b128 v[212:215], v184 offset:22528
	ds_read_b128 v[216:219], v184 offset:23552
	s_mov_b32 m0, s70
	v_lshl_add_u64 v[6:7], s[46:47], 0, v[164:165]
	global_load_lds_dwordx4 v[6:7], off
	v_lshl_add_u64 v[8:9], s[46:47], 0, v[168:169]
	s_mov_b32 m0, s71
	s_nop 0
	global_load_lds_dwordx4 v[8:9], off
	s_mov_b32 m0, s54
	v_lshl_add_u64 v[2:3], s[48:49], 0, v[162:163]
	global_load_lds_dwordx4 v[2:3], off
	v_lshl_add_u64 v[4:5], s[48:49], 0, v[166:167]
	s_mov_b32 m0, s55
	s_nop 0
	global_load_lds_dwordx4 v[4:5], off
	s_add_u32 s82, s46, 0x40000
	s_addc_u32 s83, s47, 0
	s_mov_b32 m0, s72
	v_lshl_add_u64 v[236:237], s[82:83], 0, v[164:165]
	global_load_lds_dwordx4 v[236:237], off
	v_lshl_add_u64 v[236:237], s[82:83], 0, v[168:169]
	s_mov_b32 m0, s73
	s_nop 0
	global_load_lds_dwordx4 v[236:237], off
	s_waitcnt vmcnt(8) lgkmcnt(0)
	s_barrier
	s_setprio 1
	v_mfma_f32_16x16x128_f8f6f4 v[110:113], v[10:17], v[188:195], v[110:113]
	v_mfma_f32_16x16x128_f8f6f4 v[102:105], v[174:181], v[188:195], v[102:105]
	v_mfma_f32_16x16x128_f8f6f4 v[78:81], v[10:17], v[196:203], v[78:81]
	v_mfma_f32_16x16x128_f8f6f4 v[70:73], v[174:181], v[196:203], v[70:73]
	v_mfma_f32_16x16x128_f8f6f4 v[62:65], v[10:17], v[204:211], v[62:65]
	v_mfma_f32_16x16x128_f8f6f4 v[54:57], v[174:181], v[204:211], v[54:57]
	v_mfma_f32_16x16x128_f8f6f4 v[46:49], v[10:17], v[212:219], v[46:49]
	v_mfma_f32_16x16x128_f8f6f4 v[42:45], v[174:181], v[212:219], v[42:45]
	v_mfma_f32_16x16x128_f8f6f4 v[106:109], v[220:227], v[188:195], v[106:109]
	v_mfma_f32_16x16x128_f8f6f4 v[98:101], v[228:235], v[188:195], v[98:101]
	v_mfma_f32_16x16x128_f8f6f4 v[74:77], v[220:227], v[196:203], v[74:77]
	v_mfma_f32_16x16x128_f8f6f4 v[66:69], v[228:235], v[196:203], v[66:69]
	v_mfma_f32_16x16x128_f8f6f4 v[58:61], v[220:227], v[204:211], v[58:61]
	v_mfma_f32_16x16x128_f8f6f4 v[50:53], v[228:235], v[204:211], v[50:53]
	v_mfma_f32_16x16x128_f8f6f4 v[38:41], v[220:227], v[212:219], v[38:41]
	v_mfma_f32_16x16x128_f8f6f4 v[34:37], v[228:235], v[212:219], v[34:37]
	s_setprio 0
	s_barrier
	ds_read_b128 v[10:13], v186
	ds_read_b128 v[14:17], v186 offset:1024
	ds_read_b128 v[174:177], v186 offset:2048
	ds_read_b128 v[178:181], v186 offset:3072
	s_add_u32 s48, s48, 0x40000
	s_addc_u32 s49, s49, 0
	s_mov_b32 m0, s56
	v_lshl_add_u64 v[220:221], s[48:49], 0, v[162:163]
	ds_read_b128 v[188:191], v184 offset:32768
	ds_read_b128 v[192:195], v184 offset:33792
	ds_read_b128 v[196:199], v184 offset:34816
	ds_read_b128 v[200:203], v184 offset:35840
	ds_read_b128 v[204:207], v184 offset:36864
	ds_read_b128 v[208:211], v184 offset:37888
	ds_read_b128 v[212:215], v184 offset:38912
	ds_read_b128 v[216:219], v184 offset:39936
	global_load_lds_dwordx4 v[220:221], off
	v_lshl_add_u64 v[220:221], s[48:49], 0, v[166:167]
	s_mov_b32 m0, s57
	s_nop 0
	global_load_lds_dwordx4 v[220:221], off
	ds_read_b128 v[220:223], v187
	ds_read_b128 v[224:227], v187 offset:1024
	ds_read_b128 v[228:231], v187 offset:2048
	ds_read_b128 v[232:235], v187 offset:3072
	s_waitcnt vmcnt(8) lgkmcnt(0)
	s_barrier
	s_setprio 1
	v_mfma_f32_16x16x128_f8f6f4 v[150:153], v[10:17], v[188:195], v[150:153]
	v_mfma_f32_16x16x128_f8f6f4 v[146:149], v[174:181], v[188:195], v[146:149]
	v_mfma_f32_16x16x128_f8f6f4 v[134:137], v[10:17], v[196:203], v[134:137]
	v_mfma_f32_16x16x128_f8f6f4 v[130:133], v[174:181], v[196:203], v[130:133]
	v_mfma_f32_16x16x128_f8f6f4 v[118:121], v[10:17], v[204:211], v[118:121]
	v_mfma_f32_16x16x128_f8f6f4 v[114:117], v[174:181], v[204:211], v[114:117]
	v_mfma_f32_16x16x128_f8f6f4 v[86:89], v[10:17], v[212:219], v[86:89]
	v_mfma_f32_16x16x128_f8f6f4 v[82:85], v[174:181], v[212:219], v[82:85]
	v_mfma_f32_16x16x128_f8f6f4 v[158:161], v[220:227], v[188:195], v[158:161]
	v_mfma_f32_16x16x128_f8f6f4 v[154:157], v[228:235], v[188:195], v[154:157]
	v_mfma_f32_16x16x128_f8f6f4 v[142:145], v[220:227], v[196:203], v[142:145]
	v_mfma_f32_16x16x128_f8f6f4 v[138:141], v[228:235], v[196:203], v[138:141]
	v_mfma_f32_16x16x128_f8f6f4 v[126:129], v[220:227], v[204:211], v[126:129]
	v_mfma_f32_16x16x128_f8f6f4 v[122:125], v[228:235], v[204:211], v[122:125]
	v_mfma_f32_16x16x128_f8f6f4 v[94:97], v[220:227], v[212:219], v[94:97]
	v_mfma_f32_16x16x128_f8f6f4 v[90:93], v[228:235], v[212:219], v[90:93]
	s_setprio 0
	s_barrier
	ds_read_b128 v[188:191], v184 offset:49152
	ds_read_b128 v[192:195], v184 offset:50176
	ds_read_b128 v[196:199], v184 offset:51200
	ds_read_b128 v[200:203], v184 offset:52224
	ds_read_b128 v[204:207], v184 offset:53248
	ds_read_b128 v[208:211], v184 offset:54272
	ds_read_b128 v[212:215], v184 offset:55296
	ds_read_b128 v[216:219], v184 offset:56320
	s_mov_b32 m0, s74
	v_lshl_add_u64 v[6:7], v[6:7], 0, s[10:11]
	global_load_lds_dwordx4 v[6:7], off
	v_lshl_add_u64 v[6:7], v[8:9], 0, s[10:11]
	s_mov_b32 m0, s75
	s_nop 0
	global_load_lds_dwordx4 v[6:7], off
	s_mov_b32 m0, s59
	v_lshl_add_u64 v[2:3], v[2:3], 0, s[10:11]
	global_load_lds_dwordx4 v[2:3], off
	v_lshl_add_u64 v[2:3], v[4:5], 0, s[10:11]
	s_mov_b32 m0, s60
	s_nop 0
	global_load_lds_dwordx4 v[2:3], off
	s_add_u32 s46, s46, 0x40080
	s_addc_u32 s47, s47, 0
	s_mov_b32 m0, s76
	v_lshl_add_u64 v[2:3], s[46:47], 0, v[164:165]
	global_load_lds_dwordx4 v[2:3], off
	v_lshl_add_u64 v[2:3], s[46:47], 0, v[168:169]
	s_mov_b32 m0, s77
	s_nop 0
	global_load_lds_dwordx4 v[2:3], off
	s_waitcnt vmcnt(8) lgkmcnt(0)
	s_barrier
	s_setprio 1
	v_mfma_f32_16x16x128_f8f6f4 v[110:113], v[10:17], v[188:195], v[110:113]
	v_mfma_f32_16x16x128_f8f6f4 v[102:105], v[174:181], v[188:195], v[102:105]
	v_mfma_f32_16x16x128_f8f6f4 v[78:81], v[10:17], v[196:203], v[78:81]
	v_mfma_f32_16x16x128_f8f6f4 v[70:73], v[174:181], v[196:203], v[70:73]
	v_mfma_f32_16x16x128_f8f6f4 v[62:65], v[10:17], v[204:211], v[62:65]
	v_mfma_f32_16x16x128_f8f6f4 v[54:57], v[174:181], v[204:211], v[54:57]
	v_mfma_f32_16x16x128_f8f6f4 v[46:49], v[10:17], v[212:219], v[46:49]
	v_mfma_f32_16x16x128_f8f6f4 v[42:45], v[174:181], v[212:219], v[42:45]
	v_mfma_f32_16x16x128_f8f6f4 v[106:109], v[220:227], v[188:195], v[106:109]
	v_mfma_f32_16x16x128_f8f6f4 v[98:101], v[228:235], v[188:195], v[98:101]
	v_mfma_f32_16x16x128_f8f6f4 v[74:77], v[220:227], v[196:203], v[74:77]
	v_mfma_f32_16x16x128_f8f6f4 v[66:69], v[228:235], v[196:203], v[66:69]
	v_mfma_f32_16x16x128_f8f6f4 v[58:61], v[220:227], v[204:211], v[58:61]
	v_mfma_f32_16x16x128_f8f6f4 v[50:53], v[228:235], v[204:211], v[50:53]
	v_mfma_f32_16x16x128_f8f6f4 v[38:41], v[220:227], v[212:219], v[38:41]
	v_mfma_f32_16x16x128_f8f6f4 v[34:37], v[228:235], v[212:219], v[34:37]
	s_setprio 0
	s_add_i32 s80, s80, 2
	s_add_u32 s44, s44, 0x100
	s_addc_u32 s45, s45, 0
	s_add_u32 s78, s78, 0x100
	s_addc_u32 s79, s79, 0
	s_cmp_gt_u32 s80, 13
	s_barrier
	s_cbranch_scc0 .LBB0_1547
	v_mov_b32_e32 v2, v0
	s_nop 15
	s_nop 15
	s_lshl_b32 s27, s40, 8
	v_readfirstlane_b32 s25, v2
	s_ashr_i32 s31, s25, 2
	s_andn2_b32 s31, s31, 63
	s_add_i32 s31, s31, s27
	s_lshr_b32 s25, s25, 1
	v_and_or_b32 v10, v2, 15, s31
	s_and_b32 s25, s25, 0x60
	v_lshrrev_b32_e32 v2, 1, v2
	s_lshl_b32 s27, s38, 8
	v_and_b32_e32 v4, 24, v2
	s_or_b32 s27, s25, s27
	v_or_b32_e32 v2, s27, v4
	v_ashrrev_i32_e32 v11, 31, v10
	v_ashrrev_i32_e32 v3, 31, v2
	v_lshlrev_b64 v[6:7], 12, v[10:11]
	v_lshl_add_u64 v[6:7], s[8:9], 0, v[6:7]
	v_lshlrev_b64 v[12:13], 1, v[2:3]
	s_waitcnt vmcnt(6)
	v_lshl_add_u64 v[2:3], v[6:7], 0, v[12:13]
	v_pk_fma_f32 v[6:7], v[150:151], s[18:19], v[22:23] op_sel_hi:[1,0,1]
	v_pk_fma_f32 v[8:9], v[152:153], s[18:19], v[24:25] op_sel_hi:[1,0,1]
	v_cvt_pk_bf16_f32 v6, v6, v7
	v_pk_fma_f32 v[14:15], v[148:149], s[18:19], v[20:21] op_sel_hi:[1,0,1]
	v_cvt_pk_bf16_f32 v7, v8, v9
	v_pk_fma_f32 v[16:17], v[146:147], s[18:19], v[18:19] op_sel_hi:[1,0,1]
	v_pk_fma_f32 v[130:131], v[130:131], s[18:19], v[18:19] op_sel_hi:[1,0,1]
	v_cvt_pk_bf16_f32 v8, v16, v17
	v_cvt_pk_bf16_f32 v9, v14, v15
	global_store_dwordx4 v[2:3], v[6:9], off
	v_pk_fma_f32 v[14:15], v[156:157], s[18:19], v[28:29] op_sel_hi:[1,0,1]
	v_pk_fma_f32 v[16:17], v[154:155], s[18:19], v[26:27] op_sel_hi:[1,0,1]
	v_pk_fma_f32 v[6:7], v[158:159], s[18:19], v[30:31] op_sel_hi:[1,0,1]
	v_pk_fma_f32 v[8:9], v[160:161], s[18:19], v[32:33] op_sel_hi:[1,0,1]
	v_cvt_pk_bf16_f32 v6, v6, v7
	v_pk_fma_f32 v[114:115], v[114:115], s[18:19], v[18:19] op_sel_hi:[1,0,1]
	v_cvt_pk_bf16_f32 v7, v8, v9
	v_cvt_pk_bf16_f32 v8, v16, v17
	v_cvt_pk_bf16_f32 v9, v14, v15
	global_store_dwordx4 v[2:3], v[6:9], off offset:256
	v_pk_fma_f32 v[16:17], v[132:133], s[18:19], v[20:21] op_sel_hi:[1,0,1]
	s_mov_b32 s27, 0x80000
	v_or_b32_e32 v6, 16, v10
	v_ashrrev_i32_e32 v7, 31, v6
	v_lshlrev_b64 v[6:7], 12, v[6:7]
	v_lshl_add_u64 v[6:7], s[8:9], 0, v[6:7]
	v_lshl_add_u64 v[14:15], v[6:7], 0, v[12:13]
	v_pk_fma_f32 v[6:7], v[134:135], s[18:19], v[22:23] op_sel_hi:[1,0,1]
	v_pk_fma_f32 v[8:9], v[136:137], s[18:19], v[24:25] op_sel_hi:[1,0,1]
	v_cvt_pk_bf16_f32 v6, v6, v7
	s_mov_b64 s[38:39], 0x80000
	v_cvt_pk_bf16_f32 v7, v8, v9
	v_cvt_pk_bf16_f32 v8, v130, v131
	v_cvt_pk_bf16_f32 v9, v16, v17
	global_store_dwordx4 v[14:15], v[6:9], off
	v_pk_fma_f32 v[16:17], v[140:141], s[18:19], v[28:29] op_sel_hi:[1,0,1]
	v_pk_fma_f32 v[130:131], v[138:139], s[18:19], v[26:27] op_sel_hi:[1,0,1]
	v_pk_fma_f32 v[6:7], v[142:143], s[18:19], v[30:31] op_sel_hi:[1,0,1]
	v_pk_fma_f32 v[8:9], v[144:145], s[18:19], v[32:33] op_sel_hi:[1,0,1]
	v_cvt_pk_bf16_f32 v6, v6, v7
	v_readlane_b32 s68, v254, 0
	v_cvt_pk_bf16_f32 v7, v8, v9
	v_cvt_pk_bf16_f32 v8, v130, v131
	v_cvt_pk_bf16_f32 v9, v16, v17
	global_store_dwordx4 v[14:15], v[6:9], off offset:256
	v_pk_fma_f32 v[16:17], v[116:117], s[18:19], v[20:21] op_sel_hi:[1,0,1]
	v_readlane_b32 s69, v254, 1
	v_or_b32_e32 v6, 32, v10
	v_ashrrev_i32_e32 v7, 31, v6
	v_lshlrev_b64 v[6:7], 12, v[6:7]
	v_lshl_add_u64 v[6:7], s[8:9], 0, v[6:7]
	v_lshl_add_u64 v[14:15], v[6:7], 0, v[12:13]
	v_pk_fma_f32 v[6:7], v[118:119], s[18:19], v[22:23] op_sel_hi:[1,0,1]
	v_pk_fma_f32 v[8:9], v[120:121], s[18:19], v[24:25] op_sel_hi:[1,0,1]
	v_cvt_pk_bf16_f32 v6, v6, v7
	v_readlane_b32 s70, v254, 2
	v_cvt_pk_bf16_f32 v7, v8, v9
	v_cvt_pk_bf16_f32 v8, v114, v115
	v_cvt_pk_bf16_f32 v9, v16, v17
	global_store_dwordx4 v[14:15], v[6:9], off
	v_pk_fma_f32 v[16:17], v[124:125], s[18:19], v[28:29] op_sel_hi:[1,0,1]
	v_pk_fma_f32 v[114:115], v[122:123], s[18:19], v[26:27] op_sel_hi:[1,0,1]
	v_pk_fma_f32 v[6:7], v[126:127], s[18:19], v[30:31] op_sel_hi:[1,0,1]
	v_pk_fma_f32 v[8:9], v[128:129], s[18:19], v[32:33] op_sel_hi:[1,0,1]
	v_cvt_pk_bf16_f32 v6, v6, v7
	v_readlane_b32 s71, v254, 3
	v_cvt_pk_bf16_f32 v7, v8, v9
	v_cvt_pk_bf16_f32 v8, v114, v115
	v_cvt_pk_bf16_f32 v9, v16, v17
	global_store_dwordx4 v[14:15], v[6:9], off offset:256
	v_pk_fma_f32 v[14:15], v[82:83], s[18:19], v[18:19] op_sel_hi:[1,0,1]
	v_readlane_b32 s72, v254, 4
	v_or_b32_e32 v6, 48, v10
	v_ashrrev_i32_e32 v7, 31, v6
	v_lshlrev_b64 v[6:7], 12, v[6:7]
	v_lshl_add_u64 v[6:7], s[8:9], 0, v[6:7]
	v_lshl_add_u64 v[10:11], v[6:7], 0, v[12:13]
	v_pk_fma_f32 v[8:9], v[88:89], s[18:19], v[24:25] op_sel_hi:[1,0,1]
	v_pk_fma_f32 v[6:7], v[86:87], s[18:19], v[22:23] op_sel_hi:[1,0,1]
	v_pk_fma_f32 v[12:13], v[84:85], s[18:19], v[20:21] op_sel_hi:[1,0,1]
	v_cvt_pk_bf16_f32 v6, v6, v7
	v_cvt_pk_bf16_f32 v7, v8, v9
	v_cvt_pk_bf16_f32 v8, v14, v15
	v_pk_fma_f32 v[14:15], v[90:91], s[18:19], v[26:27] op_sel_hi:[1,0,1]
	v_cvt_pk_bf16_f32 v9, v12, v13
	global_store_dwordx4 v[10:11], v[6:9], off
	v_pk_fma_f32 v[12:13], v[92:93], s[18:19], v[28:29] op_sel_hi:[1,0,1]
	v_readfirstlane_b32 s99, v0
	s_cmpk_gt_u32 s99, 0xff
	s_cbranch_scc1 .Lz0_1547
	s_barrier
.Lz0_1547:
	v_readlane_b32 s73, v254, 5
	v_pk_fma_f32 v[8:9], v[96:97], s[18:19], v[32:33] op_sel_hi:[1,0,1]
	v_pk_fma_f32 v[6:7], v[94:95], s[18:19], v[30:31] op_sel_hi:[1,0,1]
	v_readlane_b32 s74, v254, 6
	v_cvt_pk_bf16_f32 v6, v6, v7
	v_cvt_pk_bf16_f32 v7, v8, v9
	v_cvt_pk_bf16_f32 v8, v14, v15
	v_cvt_pk_bf16_f32 v9, v12, v13
	global_store_dwordx4 v[10:11], v[6:9], off offset:256
	v_pk_fma_f32 v[12:13], v[104:105], s[18:19], v[20:21] op_sel_hi:[1,0,1]
	v_pk_fma_f32 v[14:15], v[102:103], s[18:19], v[18:19] op_sel_hi:[1,0,1]
	v_pk_fma_f32 v[8:9], v[112:113], s[18:19], v[24:25] op_sel_hi:[1,0,1]
	v_pk_fma_f32 v[6:7], v[110:111], s[18:19], v[22:23] op_sel_hi:[1,0,1]
	v_lshl_add_u64 v[10:11], v[2:3], 0, s[38:39]
	v_cvt_pk_bf16_f32 v6, v6, v7
	v_cvt_pk_bf16_f32 v7, v8, v9
	v_cvt_pk_bf16_f32 v8, v14, v15
	v_cvt_pk_bf16_f32 v9, v12, v13
	v_add_co_u32_e32 v12, vcc, s27, v2
	v_pk_fma_f32 v[14:15], v[98:99], s[18:19], v[26:27] op_sel_hi:[1,0,1]
	s_nop 0
	v_addc_co_u32_e32 v13, vcc, 0, v3, vcc
	global_store_dwordx4 v[12:13], v[6:9], off
	v_pk_fma_f32 v[12:13], v[100:101], s[18:19], v[28:29] op_sel_hi:[1,0,1]
	s_mov_b32 s27, 0x90000
	v_pk_fma_f32 v[8:9], v[108:109], s[18:19], v[32:33] op_sel_hi:[1,0,1]
	v_pk_fma_f32 v[6:7], v[106:107], s[18:19], v[30:31] op_sel_hi:[1,0,1]
	s_mov_b64 s[38:39], 0x90000
	v_cvt_pk_bf16_f32 v6, v6, v7
	v_cvt_pk_bf16_f32 v7, v8, v9
	v_cvt_pk_bf16_f32 v8, v14, v15
	v_cvt_pk_bf16_f32 v9, v12, v13
	global_store_dwordx4 v[10:11], v[6:9], off offset:256
	v_pk_fma_f32 v[12:13], v[72:73], s[18:19], v[20:21] op_sel_hi:[1,0,1]
	v_pk_fma_f32 v[14:15], v[70:71], s[18:19], v[18:19] op_sel_hi:[1,0,1]
	v_pk_fma_f32 v[8:9], v[80:81], s[18:19], v[24:25] op_sel_hi:[1,0,1]
	v_pk_fma_f32 v[6:7], v[78:79], s[18:19], v[22:23] op_sel_hi:[1,0,1]
	v_lshl_add_u64 v[10:11], v[2:3], 0, s[38:39]
	v_cvt_pk_bf16_f32 v6, v6, v7
	v_cvt_pk_bf16_f32 v7, v8, v9
	v_cvt_pk_bf16_f32 v8, v14, v15
	v_cvt_pk_bf16_f32 v9, v12, v13
	v_add_co_u32_e32 v12, vcc, s27, v2
	v_pk_fma_f32 v[14:15], v[66:67], s[18:19], v[26:27] op_sel_hi:[1,0,1]
	s_nop 0
	v_addc_co_u32_e32 v13, vcc, 0, v3, vcc
	global_store_dwordx4 v[12:13], v[6:9], off
	v_pk_fma_f32 v[12:13], v[68:69], s[18:19], v[28:29] op_sel_hi:[1,0,1]
	s_mov_b64 s[38:39], 0xa0000
	v_pk_fma_f32 v[8:9], v[76:77], s[18:19], v[32:33] op_sel_hi:[1,0,1]
	v_pk_fma_f32 v[6:7], v[74:75], s[18:19], v[30:31] op_sel_hi:[1,0,1]
	v_readlane_b32 s75, v254, 7
	v_cvt_pk_bf16_f32 v6, v6, v7
	v_cvt_pk_bf16_f32 v7, v8, v9
	v_cvt_pk_bf16_f32 v8, v14, v15
	v_cvt_pk_bf16_f32 v9, v12, v13
	global_store_dwordx4 v[10:11], v[6:9], off offset:256
	v_pk_fma_f32 v[12:13], v[56:57], s[18:19], v[20:21] op_sel_hi:[1,0,1]
	v_pk_fma_f32 v[14:15], v[54:55], s[18:19], v[18:19] op_sel_hi:[1,0,1]
	v_pk_fma_f32 v[8:9], v[64:65], s[18:19], v[24:25] op_sel_hi:[1,0,1]
	v_pk_fma_f32 v[6:7], v[62:63], s[18:19], v[22:23] op_sel_hi:[1,0,1]
	v_lshl_add_u64 v[10:11], v[2:3], 0, s[38:39]
	v_cvt_pk_bf16_f32 v6, v6, v7
	v_cvt_pk_bf16_f32 v7, v8, v9
	v_cvt_pk_bf16_f32 v8, v14, v15
	v_cvt_pk_bf16_f32 v9, v12, v13
	v_add_co_u32_e32 v12, vcc, s66, v2
	v_pk_fma_f32 v[14:15], v[50:51], s[18:19], v[26:27] op_sel_hi:[1,0,1]
	s_nop 0
	v_addc_co_u32_e32 v13, vcc, 0, v3, vcc
	global_store_dwordx4 v[12:13], v[6:9], off
	v_pk_fma_f32 v[12:13], v[52:53], s[18:19], v[28:29] op_sel_hi:[1,0,1]
	s_mov_b64 s[38:39], -1
	v_pk_fma_f32 v[8:9], v[60:61], s[18:19], v[32:33] op_sel_hi:[1,0,1]
	v_pk_fma_f32 v[6:7], v[58:59], s[18:19], v[30:31] op_sel_hi:[1,0,1]
	s_nop 0
	v_cvt_pk_bf16_f32 v6, v6, v7
	v_cvt_pk_bf16_f32 v7, v8, v9
	v_cvt_pk_bf16_f32 v8, v14, v15
	v_cvt_pk_bf16_f32 v9, v12, v13
	global_store_dwordx4 v[10:11], v[6:9], off offset:256
	v_lshl_add_u64 v[10:11], v[2:3], 0, s[20:21]
	v_add_co_u32_e32 v2, vcc, s67, v2
	v_pk_fma_f32 v[8:9], v[48:49], s[18:19], v[24:25] op_sel_hi:[1,0,1]
	v_pk_fma_f32 v[6:7], v[46:47], s[18:19], v[22:23] op_sel_hi:[1,0,1]
	v_pk_fma_f32 v[12:13], v[44:45], s[18:19], v[20:21] op_sel_hi:[1,0,1]
	v_pk_fma_f32 v[14:15], v[42:43], s[18:19], v[18:19] op_sel_hi:[1,0,1]
	v_cvt_pk_bf16_f32 v6, v6, v7
	v_cvt_pk_bf16_f32 v7, v8, v9
	v_addc_co_u32_e32 v3, vcc, 0, v3, vcc
	v_cvt_pk_bf16_f32 v8, v14, v15
	v_cvt_pk_bf16_f32 v9, v12, v13
	global_store_dwordx4 v[2:3], v[6:9], off
	s_and_b64 vcc, s[42:43], exec
	v_pk_fma_f32 v[2:3], v[40:41], s[18:19], v[32:33] op_sel_hi:[1,0,1]
	v_pk_fma_f32 v[6:7], v[38:39], s[18:19], v[30:31] op_sel_hi:[1,0,1]
	v_pk_fma_f32 v[8:9], v[34:35], s[18:19], v[26:27] op_sel_hi:[1,0,1]
	v_pk_fma_f32 v[12:13], v[36:37], s[18:19], v[28:29] op_sel_hi:[1,0,1]
	v_cvt_pk_bf16_f32 v6, v6, v7
	v_cvt_pk_bf16_f32 v7, v2, v3
	v_cvt_pk_bf16_f32 v8, v8, v9
	s_nop 0
	v_cvt_pk_bf16_f32 v9, v12, v13
	global_store_dwordx4 v[10:11], v[6:9], off offset:256
	v_readfirstlane_b32 s99, v0
	s_cmpk_gt_u32 s99, 0xff
	s_cbranch_scc0 .Lz1_1547
	s_barrier
